# bf16 GEMMs (in-proj, out-proj): LDS-DMA pieces reshaped to 8 rows x 128 B with swizzled row-major LDS image; second k-step read through base^64
# baseline (speedup 1.0000x reference)
.LBB0_232:
	s_andn2_b64 vcc, exec, s[0:1]
	s_cbranch_vccnz .LBB0_217
	s_mov_b32 s2, 0
	s_andn2_b64 vcc, exec, s[16:17]
	v_mbcnt_lo_u32_b32 v0, -1, 0
	v_mbcnt_hi_u32_b32 v0, -1, v0
	s_cbranch_vccnz .LBB0_288
	v_add_u32_e32 v1, s33, v0
	v_lshlrev_b32_e32 v2, 4, v1
	v_add_u32_e32 v3, 0x2000, v2
	v_ashrrev_i32_e32 v4, 31, v3
	v_lshrrev_b32_e32 v4, 22, v4
	v_add_u32_e32 v4, v3, v4
	v_ashrrev_i32_e32 v4, 10, v4
	v_mul_i32_i24_e32 v5, 0x400, v4
	v_sub_u32_e32 v3, v3, v5
	v_lshrrev_b32_e32 v5, 4, v3
	v_bitop3_b32 v3, v5, v3, 32 bitop3:0x6c
	v_ashrrev_i32_e32 v5, 31, v3
	v_lshrrev_b32_e32 v5, 26, v5
	v_add_u32_e32 v5, v3, v5
	v_lshlrev_b32_e32 v7, 3, v4
	v_ashrrev_i32_e32 v6, 6, v5
	v_and_b32_e32 v7, -16, v7
	v_add_u32_e32 v7, v6, v7
	v_lshlrev_b32_e32 v8, 1, v7
	v_and_b32_e32 v9, 0x7ffe0, v7
	v_lshrrev_b32_e32 v7, 2, v7
	v_and_b32_e32 v6, 3, v6
	v_and_b32_e32 v5, 0xc0, v5
	v_and_or_b32 v6, v7, 4, v6
	v_lshlrev_b32_e32 v4, 5, v4
	v_sub_u32_e32 v3, v3, v5
	v_and_or_b32 v8, v8, 24, v9
	v_lshlrev_b32_e32 v6, 12, v6
	v_and_b32_e32 v4, 32, v4
	v_ashrrev_i16_sdwa v3, v176, sext(v3) dst_sel:DWORD dst_unused:UNUSED_PAD src0_sel:DWORD src1_sel:BYTE_0
	v_lshl_or_b32 v6, v8, 13, v6
	v_add_u32_sdwa v3, v4, sext(v3) dst_sel:DWORD dst_unused:UNUSED_PAD src0_sel:DWORD src1_sel:WORD_0
	v_lshl_add_u32 v162, v3, 1, v6
	v_bfe_i32 v3, v1, 27, 1
	v_lshrrev_b32_e32 v3, 22, v3
	v_add_u32_e32 v3, v2, v3
	v_and_b32_e32 v3, 0xfffffc00, v3
	v_sub_u32_e32 v2, v2, v3
	v_lshrrev_b32_e32 v3, 4, v2
	v_ashrrev_i32_e32 v5, 31, v1
	v_bitop3_b32 v2, v3, v2, 32 bitop3:0x6c
	v_lshrrev_b32_e32 v5, 26, v5
	v_ashrrev_i32_e32 v3, 31, v2
	v_add_u32_e32 v1, v1, v5
	v_lshrrev_b32_e32 v3, 26, v3
	v_ashrrev_i32_e32 v1, 6, v1
	v_add_u32_e32 v3, v2, v3
	v_lshlrev_b32_e32 v5, 3, v1
	v_ashrrev_i32_e32 v4, 6, v3
	v_and_b32_e32 v5, -16, v5
	v_readlane_b32 s2, v254, 13
	v_add_u32_e32 v5, v4, v5
	v_readlane_b32 s3, v254, 14
	v_lshlrev_b32_e32 v6, 1, v5
	v_and_b32_e32 v7, 0x7ffe0, v5
	v_lshrrev_b32_e32 v5, 2, v5
	v_and_b32_e32 v4, 3, v4
	v_and_b32_e32 v3, 0xc0, v3
	s_mov_b64 s[0:1], s[2:3]
	v_and_or_b32 v4, v5, 4, v4
	v_lshlrev_b32_e32 v1, 5, v1
	v_sub_u32_e32 v2, v2, v3
	v_and_or_b32 v6, v6, 24, v7
	v_lshlrev_b32_e32 v4, 12, v4
	v_and_b32_e32 v1, 32, v1
	v_ashrrev_i16_sdwa v2, v176, sext(v2) dst_sel:DWORD dst_unused:UNUSED_PAD src0_sel:DWORD src1_sel:BYTE_0
	s_load_dwordx2 s[70:71], s[0:1], 0xc0
	s_mov_b64 s[0:1], s[2:3]
	v_lshl_or_b32 v4, v6, 13, v4
	v_add_u32_sdwa v1, v1, sext(v2) dst_sel:DWORD dst_unused:UNUSED_PAD src0_sel:DWORD src1_sel:WORD_0
	v_lshl_add_u32 v160, v1, 1, v4
	v_add_u32_e32 v1, s33, v0
	v_lshrrev_b32_e32 v2, 3, v1
	v_and_b32_e32 v1, 7, v1
	v_bfe_u32 v3, v2, 1, 3
	v_and_b32_e32 v4, 1, v3
	v_lshlrev_b32_e32 v4, 1, v4
	v_and_or_b32 v3, v3, 4, v4
	v_xor_b32_e32 v1, v1, v3
	v_lshlrev_b32_e32 v1, 4, v1
	v_lshrrev_b32_e32 v3, 5, v2
	v_lshlrev_b32_e32 v3, 6, v3
	v_bfe_u32 v4, v2, 2, 2
	v_lshl_or_b32 v3, v4, 4, v3
	v_bfe_u32 v4, v2, 4, 1
	v_lshl_or_b32 v3, v4, 2, v3
	v_and_b32_e32 v4, 3, v2
	v_or_b32_e32 v3, v3, v4
	v_lshl_add_u32 v160, v3, 12, v1
	v_add_u32_e32 v162, 0x80000, v160
	s_load_dwordx2 s[0:1], s[0:1], 0xc0
	s_waitcnt lgkmcnt(0)
	s_barrier
	v_mbcnt_lo_u32_b32 v1, -1, 0
	v_mbcnt_hi_u32_b32 v1, -1, v1
	s_waitcnt lgkmcnt(0)
	s_add_u32 s0, s0, s26
	v_add_u32_e32 v1, s33, v1
	v_ashrrev_i32_e32 v3, 31, v1
	v_lshrrev_b32_e32 v3, 26, v3
	v_lshlrev_b32_e32 v2, 4, v1
	v_add_u32_e32 v3, v1, v3
	v_bfe_i32 v1, v1, 27, 1
	v_lshrrev_b32_e32 v1, 22, v1
	v_add_u32_e32 v1, v2, v1
	v_and_b32_e32 v1, 0xfffffc00, v1
	v_sub_u32_e32 v1, v2, v1
	v_lshrrev_b32_e32 v4, 4, v1
	v_bitop3_b32 v1, v4, v1, 32 bitop3:0x6c
	v_ashrrev_i32_e32 v5, 31, v1
	v_lshrrev_b32_e32 v5, 26, v5
	v_add_u32_e32 v5, v1, v5
	v_ashrrev_i32_e32 v6, 6, v5
	v_and_b32_e32 v5, 0xc0, v5
	v_ashrrev_i32_e32 v3, 6, v3
	v_sub_u32_e32 v1, v1, v5
	v_lshlrev_b32_e32 v4, 3, v3
	v_lshlrev_b32_e32 v3, 5, v3
	v_ashrrev_i16_sdwa v1, v176, sext(v1) dst_sel:DWORD dst_unused:UNUSED_PAD src0_sel:DWORD src1_sel:BYTE_0
	v_and_b32_e32 v3, 32, v3
	v_bfe_i32 v1, v1, 0, 16
	v_add_u32_e32 v2, 0x2000, v2
	v_add_lshl_u32 v1, v3, v1, 1
	v_ashrrev_i32_e32 v3, 31, v2
	v_lshrrev_b32_e32 v3, 22, v3
	v_add_u32_e32 v3, v2, v3
	v_ashrrev_i32_e32 v3, 10, v3
	v_mul_i32_i24_e32 v5, 0x400, v3
	v_sub_u32_e32 v2, v2, v5
	v_lshrrev_b32_e32 v5, 4, v2
	v_and_b32_e32 v4, -16, v4
	v_bitop3_b32 v2, v5, v2, 32 bitop3:0x6c
	s_addc_u32 s1, s1, s27
	v_add_u32_e32 v4, v6, v4
	v_ashrrev_i32_e32 v6, 31, v2
	s_add_u32 s6, s0, 0x400000
	v_lshrrev_b32_e32 v6, 26, v6
	s_addc_u32 s7, s1, 0
	s_add_i32 s97, s61, 0
	v_add_u32_e32 v6, v2, v6
	s_add_i32 m0, s97, 0x10000
	v_ashrrev_i32_e32 v7, 6, v6
	v_and_b32_e32 v6, 0xc0, v6
	v_sub_u32_e32 v2, v2, v6
	global_load_lds_dwordx4 v160, s[6:7]
	s_add_i32 m0, s97, 0x12000
	s_add_u32 s0, s0, 0x408000
	v_lshlrev_b32_e32 v5, 3, v3
	v_lshlrev_b32_e32 v3, 5, v3
	v_ashrrev_i16_sdwa v2, v176, sext(v2) dst_sel:DWORD dst_unused:UNUSED_PAD src0_sel:DWORD src1_sel:BYTE_0
	s_addc_u32 s1, s1, 0
	global_load_lds_dwordx4 v162, s[6:7]
	s_add_i32 m0, s97, 0x14000
	v_and_b32_e32 v5, -16, v5
	v_and_b32_e32 v3, 32, v3
	v_bfe_i32 v2, v2, 0, 16
	v_add_u32_e32 v5, v7, v5
	global_load_lds_dwordx4 v160, s[0:1]
	s_add_i32 m0, s97, 0x16000
	v_add_lshl_u32 v2, v3, v2, 1
	v_add_u32_e32 v6, s33, v0
	v_lshrrev_b32_e32 v4, 3, v6
	v_add_u32_e32 v5, 64, v4
	v_and_b32_e32 v1, 7, v0
	v_bfe_u32 v6, v4, 1, 3
	v_and_b32_e32 v7, 1, v6
	v_lshlrev_b32_e32 v7, 1, v7
	v_and_or_b32 v6, v6, 4, v7
	v_xor_b32_e32 v1, v1, v6
	v_lshlrev_b32_e32 v1, 4, v1
	v_mov_b32_e32 v2, v1
	v_lshlrev_b32_e32 v3, 12, v4
	s_add_u32 s72, s70, 0x32000000
	v_add3_u32 v164, v3, s85, v1
	v_lshlrev_b32_e32 v3, 12, v5
	s_addc_u32 s73, s71, 0
	global_load_lds_dwordx4 v162, s[0:1]
	s_mov_b32 m0, s97
	s_add_i32 s28, s97, 0x2000
	v_add3_u32 v166, v3, s85, v2
	v_add_u32_e32 v3, s86, v4
	s_add_i32 s29, s97, 0x4000
	global_load_lds_dwordx4 v164, s[72:73]
	s_mov_b32 m0, s28
	v_lshl_add_u32 v1, v3, 12, v1
	v_add_u32_e32 v3, s86, v5
	s_add_i32 s30, s97, 0x6000
	global_load_lds_dwordx4 v166, s[72:73]
	s_mov_b32 m0, s29
	v_lshl_add_u32 v170, v3, 12, v2
	v_cndmask_b32_e64 v2, 0, 1, s[18:19]
	global_load_lds_dwordx4 v1, s[72:73]
	s_mov_b32 m0, s30
	v_cmp_ne_u32_e64 s[2:3], 1, v2
	global_load_lds_dwordx4 v170, s[72:73]
	s_andn2_b64 vcc, exec, s[18:19]
	s_cbranch_vccnz .LBB0_236
	s_barrier
.LBB0_236:
	v_and_b32_e32 v2, 15, v0
	v_or_b32_e32 v3, s63, v2
	v_lshlrev_b32_e32 v6, 4, v0
	v_lshlrev_b32_e32 v4, 6, v3
	v_and_b32_e32 v5, 48, v0
	s_movk_i32 s0, 0x3c0
	v_and_b32_e32 v6, 0xfffffc00, v6
	v_lshlrev_b32_e32 v3, 2, v3
	v_and_or_b32 v4, v4, s0, v5
	v_add_u32_e32 v7, s65, v6
	v_and_b32_e32 v3, 32, v3
	v_lshlrev_b32_e32 v0, 2, v0
	v_bitop3_b32 v4, v4, v7, v3 bitop3:0xde
	v_lshl_or_b32 v2, v2, 6, v5
	v_add_u32_e32 v3, s67, v6
	v_and_b32_e32 v0, 32, v0
	v_bitop3_b32 v177, v2, v3, v0 bitop3:0xde
	v_mbcnt_lo_u32_b32 v0, -1, 0
	v_mbcnt_hi_u32_b32 v0, -1, v0
	v_and_b32_e32 v5, 15, v0
	v_lshrrev_b32_e32 v0, 4, v0
	v_bfe_u32 v6, v5, 1, 3
	v_and_b32_e32 v7, 1, v6
	v_lshlrev_b32_e32 v7, 1, v7
	v_and_or_b32 v6, v6, 4, v7
	v_xor_b32_e32 v0, v0, v6
	v_lshlrev_b32_e32 v0, 4, v0
	v_lshl_add_u32 v0, v5, 7, v0
	v_add_u32_e32 v4, s65, v0
	v_xor_b32_e32 v212, 64, v4
	v_add_u32_e32 v177, s67, v0
	v_xor_b32_e32 v213, 64, v177
	v_add_u32_e32 v213, 0x10000, v213
	s_waitcnt vmcnt(2)
	s_barrier
	s_add_i32 m0, s97, 0x18000
	v_lshl_add_u64 v[2:3], s[6:7], 0, v[160:161]
	v_lshl_add_u64 v[2:3], v[2:3], 0, s[52:53]
	global_load_lds_dwordx4 v[2:3], off
	v_mov_b32_e32 v163, v161
	s_add_i32 m0, s97, 0x1a000
	s_add_u32 s0, s70, 0x32000080
	v_lshl_add_u64 v[2:3], s[6:7], 0, v[162:163]
	v_lshl_add_u64 v[2:3], v[2:3], 0, s[52:53]
	s_addc_u32 s1, s71, 0
	s_add_i32 s31, s97, 0x8000
	global_load_lds_dwordx4 v[2:3], off
	s_mov_b32 m0, s31
	s_add_i32 s42, s97, 0xa000
	v_mov_b32_e32 v0, 0
	global_load_lds_dwordx4 v164, s[0:1]
	s_mov_b32 m0, s42
	s_mov_b32 s47, 0
	global_load_lds_dwordx4 v166, s[0:1]
	s_add_u32 s0, s6, 0x8080
	s_addc_u32 s1, s7, 0
	s_add_i32 m0, s97, 0x1c000
	v_add_u32_e32 v178, 0, v4
	global_load_lds_dwordx4 v160, s[0:1]
	s_add_i32 m0, s97, 0x1e000
	v_mov_b32_e32 v168, v160
	global_load_lds_dwordx4 v162, s[0:1]
	s_waitcnt vmcnt(6)
	v_mov_b32_e32 v160, v1
	s_mov_b32 s43, s82
	s_mov_b32 s83, s44
	v_mov_b32_e32 v1, v0
	v_mov_b32_e32 v2, v0
	v_mov_b32_e32 v3, v0
	v_mov_b32_e32 v4, v0
	v_mov_b32_e32 v5, v0
	v_mov_b32_e32 v6, v0
	v_mov_b32_e32 v7, v0
	v_mov_b32_e32 v8, v0
	v_mov_b32_e32 v9, v0
	v_mov_b32_e32 v10, v0
	v_mov_b32_e32 v11, v0
	v_mov_b32_e32 v12, v0
	v_mov_b32_e32 v13, v0
	v_mov_b32_e32 v14, v0
	v_mov_b32_e32 v15, v0
	v_mov_b32_e32 v16, v0
	v_mov_b32_e32 v17, v0
	v_mov_b32_e32 v18, v0
	v_mov_b32_e32 v19, v0
	v_mov_b32_e32 v20, v0
	v_mov_b32_e32 v21, v0
	v_mov_b32_e32 v22, v0
	v_mov_b32_e32 v23, v0
	v_mov_b32_e32 v24, v0
	v_mov_b32_e32 v25, v0
	v_mov_b32_e32 v26, v0
	v_mov_b32_e32 v27, v0
	v_mov_b32_e32 v28, v0
	v_mov_b32_e32 v29, v0
	v_mov_b32_e32 v30, v0
	v_mov_b32_e32 v31, v0
	v_mov_b32_e32 v36, v0
	v_mov_b32_e32 v37, v0
	v_mov_b32_e32 v38, v0
	v_mov_b32_e32 v39, v0
	v_mov_b32_e32 v44, v0
	v_mov_b32_e32 v45, v0
	v_mov_b32_e32 v46, v0
	v_mov_b32_e32 v47, v0
	v_mov_b32_e32 v32, v0
	v_mov_b32_e32 v33, v0
	v_mov_b32_e32 v34, v0
	v_mov_b32_e32 v35, v0
	v_mov_b32_e32 v40, v0
	v_mov_b32_e32 v41, v0
	v_mov_b32_e32 v42, v0
	v_mov_b32_e32 v43, v0
	v_mov_b32_e32 v48, v0
	v_mov_b32_e32 v49, v0
	v_mov_b32_e32 v50, v0
	v_mov_b32_e32 v51, v0
	v_mov_b32_e32 v52, v0
	v_mov_b32_e32 v53, v0
	v_mov_b32_e32 v54, v0
	v_mov_b32_e32 v55, v0
	v_mov_b32_e32 v56, v0
	v_mov_b32_e32 v57, v0
	v_mov_b32_e32 v58, v0
	v_mov_b32_e32 v59, v0
	v_mov_b32_e32 v60, v0
	v_mov_b32_e32 v61, v0
	v_mov_b32_e32 v62, v0
	v_mov_b32_e32 v63, v0
	v_mov_b32_e32 v64, v0
	v_mov_b32_e32 v65, v0
	v_mov_b32_e32 v66, v0
	v_mov_b32_e32 v67, v0
	v_mov_b32_e32 v68, v0
	v_mov_b32_e32 v69, v0
	v_mov_b32_e32 v70, v0
	v_mov_b32_e32 v71, v0
	v_mov_b32_e32 v72, v0
	v_mov_b32_e32 v73, v0
	v_mov_b32_e32 v74, v0
	v_mov_b32_e32 v75, v0
	v_mov_b32_e32 v76, v0
	v_mov_b32_e32 v77, v0
	v_mov_b32_e32 v78, v0
	v_mov_b32_e32 v79, v0
	v_mov_b32_e32 v80, v0
	v_mov_b32_e32 v81, v0
	v_mov_b32_e32 v82, v0
	v_mov_b32_e32 v83, v0
	v_mov_b32_e32 v84, v0
	v_mov_b32_e32 v85, v0
	v_mov_b32_e32 v86, v0
	v_mov_b32_e32 v87, v0
	v_mov_b32_e32 v88, v0
	v_mov_b32_e32 v89, v0
	v_mov_b32_e32 v90, v0
	v_mov_b32_e32 v91, v0
	v_mov_b32_e32 v92, v0
	v_mov_b32_e32 v93, v0
	v_mov_b32_e32 v94, v0
	v_mov_b32_e32 v95, v0
	v_mov_b32_e32 v96, v0
	v_mov_b32_e32 v97, v0
	v_mov_b32_e32 v98, v0
	v_mov_b32_e32 v99, v0
	v_mov_b32_e32 v100, v0
	v_mov_b32_e32 v101, v0
	v_mov_b32_e32 v102, v0
	v_mov_b32_e32 v103, v0
	v_mov_b32_e32 v104, v0
	v_mov_b32_e32 v105, v0
	v_mov_b32_e32 v106, v0
	v_mov_b32_e32 v107, v0
	v_mov_b32_e32 v108, v0
	v_mov_b32_e32 v109, v0
	v_mov_b32_e32 v110, v0
	v_mov_b32_e32 v111, v0
	v_mov_b32_e32 v112, v0
	v_mov_b32_e32 v113, v0
	v_mov_b32_e32 v114, v0
	v_mov_b32_e32 v115, v0
	v_mov_b32_e32 v116, v0
	v_mov_b32_e32 v117, v0
	v_mov_b32_e32 v118, v0
	v_mov_b32_e32 v119, v0
	v_mov_b32_e32 v120, v0
	v_mov_b32_e32 v121, v0
	v_mov_b32_e32 v122, v0
	v_mov_b32_e32 v123, v0
	v_mov_b32_e32 v124, v0
	v_mov_b32_e32 v125, v0
	v_mov_b32_e32 v126, v0
	v_mov_b32_e32 v127, v0
	s_barrier

.LBB0_243:
	s_add_u32 s75, s6, 0x100
	s_addc_u32 s48, s7, 0
	s_lshl_b32 s49, s45, 8
	s_lshl_b32 s8, s45, 20
	s_bitset1_b32 s49, 7
	s_mov_b32 s80, -2
	s_mov_b64 s[6:7], 0
	s_cmp_eq_u32 s80, 28
	s_cselect_b64 s[34:35], -1, 0
	s_and_b64 s[24:25], s[0:1], s[34:35]
	s_andn2_b64 vcc, exec, s[24:25]
	v_mov_b32_e32 v128, v170
	v_mov_b32_e32 v129, v160
	s_add_u32 vcc_lo, s70, s6
	s_addc_u32 vcc_hi, s71, s7
	s_add_u32 s81, vcc_lo, 0x32000100
	s_addc_u32 s50, vcc_hi, 0
	s_and_b64 s[24:25], s[34:35], exec
	s_cselect_b32 s25, s73, s50
	s_cselect_b32 s24, s72, s81
	s_add_u32 s50, s75, s6
	s_addc_u32 s51, s48, s7
	s_and_b64 s[34:35], s[34:35], exec
	s_cselect_b32 s35, s79, s51
	s_cselect_b32 s34, s78, s50
	s_add_i32 s50, 0, 0x10000
	s_add_i32 s51, 0, 0x14000
	v_add_u32_e32 v142, s50, v177
	v_add_u32_e32 v158, s51, v177
	ds_read_b128 v[130:133], v142
	ds_read_b128 v[134:137], v213
	ds_read_b128 v[138:141], v142 offset:2048
	ds_read_b128 v[142:145], v213 offset:2048
	ds_read_b128 v[146:149], v158
	ds_read_b128 v[150:153], v213 offset:16384
	ds_read_b128 v[154:157], v158 offset:2048
	ds_read_b128 v[172:175], v213 offset:18432
	ds_read_b128 v[180:183], v178
	ds_read_b128 v[184:187], v212
	ds_read_b128 v[188:191], v178 offset:2048
	ds_read_b128 v[192:195], v212 offset:2048
	ds_read_b128 v[196:199], v178 offset:4096
	ds_read_b128 v[200:203], v212 offset:4096
	ds_read_b128 v[204:207], v178 offset:6144
	ds_read_b128 v[208:211], v212 offset:6144
	s_add_i32 m0, s97, 0xc000
	v_lshl_add_u64 v[158:159], vcc, 0, v[160:161]
	v_lshl_add_u64 v[158:159], v[158:159], 0, s[54:55]
	v_mov_b32_e32 v171, v161
	global_load_lds_dwordx4 v[158:159], off
	s_add_i32 m0, s97, 0xe000
	v_lshl_add_u64 v[158:159], vcc, 0, v[170:171]
	v_lshl_add_u64 v[158:159], v[158:159], 0, s[54:55]
	global_load_lds_dwordx4 v[158:159], off
	s_waitcnt vmcnt(8)
	s_waitcnt lgkmcnt(0)
	s_barrier
	s_setprio 1
	s_waitcnt lgkmcnt(0)
	v_mfma_f32_16x16x32_bf16 v[100:103], v[130:133], v[180:183], 0
	v_mfma_f32_16x16x32_bf16 v[96:99], v[138:141], v[180:183], 0
	v_mfma_f32_16x16x32_bf16 v[92:95], v[130:133], v[188:191], 0
	v_mfma_f32_16x16x32_bf16 v[88:91], v[138:141], v[188:191], 0
	v_mfma_f32_16x16x32_bf16 v[84:87], v[130:133], v[196:199], 0
	v_mfma_f32_16x16x32_bf16 v[80:83], v[138:141], v[196:199], 0
	v_mfma_f32_16x16x32_bf16 v[76:79], v[130:133], v[204:207], 0
	v_mfma_f32_16x16x32_bf16 v[72:75], v[138:141], v[204:207], 0
	v_mfma_f32_16x16x32_bf16 v[100:103], v[134:137], v[184:187], v[100:103]
	v_mfma_f32_16x16x32_bf16 v[96:99], v[142:145], v[184:187], v[96:99]
	v_mfma_f32_16x16x32_bf16 v[92:95], v[134:137], v[192:195], v[92:95]
	v_mfma_f32_16x16x32_bf16 v[88:91], v[142:145], v[192:195], v[88:91]
	v_mfma_f32_16x16x32_bf16 v[84:87], v[134:137], v[200:203], v[84:87]
	v_mfma_f32_16x16x32_bf16 v[80:83], v[142:145], v[200:203], v[80:83]
	v_mfma_f32_16x16x32_bf16 v[76:79], v[134:137], v[208:211], v[76:79]
	v_mfma_f32_16x16x32_bf16 v[72:75], v[142:145], v[208:211], v[72:75]
	s_setprio 0
	s_setprio 1
	v_mfma_f32_16x16x32_bf16 v[68:71], v[146:149], v[180:183], 0
	v_mfma_f32_16x16x32_bf16 v[64:67], v[154:157], v[180:183], 0
	v_mfma_f32_16x16x32_bf16 v[60:63], v[146:149], v[188:191], 0
	v_mfma_f32_16x16x32_bf16 v[56:59], v[154:157], v[188:191], 0
	v_mfma_f32_16x16x32_bf16 v[52:55], v[146:149], v[196:199], 0
	v_mfma_f32_16x16x32_bf16 v[48:51], v[154:157], v[196:199], 0
	v_mfma_f32_16x16x32_bf16 v[40:43], v[146:149], v[204:207], 0
	v_mfma_f32_16x16x32_bf16 v[32:35], v[154:157], v[204:207], 0
	v_mfma_f32_16x16x32_bf16 v[68:71], v[150:153], v[184:187], v[68:71]
	v_mfma_f32_16x16x32_bf16 v[64:67], v[172:175], v[184:187], v[64:67]
	v_mfma_f32_16x16x32_bf16 v[60:63], v[150:153], v[192:195], v[60:63]
	v_mfma_f32_16x16x32_bf16 v[56:59], v[172:175], v[192:195], v[56:59]
	v_mfma_f32_16x16x32_bf16 v[52:55], v[150:153], v[200:203], v[52:55]
	v_mfma_f32_16x16x32_bf16 v[48:51], v[172:175], v[200:203], v[48:51]
	v_mfma_f32_16x16x32_bf16 v[40:43], v[150:153], v[208:211], v[40:43]
	v_mfma_f32_16x16x32_bf16 v[32:35], v[172:175], v[208:211], v[32:35]
	s_setprio 0
	s_barrier
	s_add_i32 s50, s50, s61
	s_mov_b32 m0, s50
	ds_read_b128 v[180:183], v178 offset:16384
	ds_read_b128 v[184:187], v212 offset:16384
	ds_read_b128 v[188:191], v178 offset:18432
	ds_read_b128 v[192:195], v212 offset:18432
	ds_read_b128 v[196:199], v178 offset:20480
	ds_read_b128 v[200:203], v212 offset:20480
	ds_read_b128 v[204:207], v178 offset:22528
	ds_read_b128 v[208:211], v212 offset:22528
	s_nop 0
	global_load_lds_dwordx4 v168, s[34:35]
	s_add_i32 m0, s50, 0x2000
	s_add_u32 vcc_lo, s34, 0x8000
	s_addc_u32 vcc_hi, s35, 0
	s_add_i32 s50, s51, s61
	s_nop 0
	global_load_lds_dwordx4 v162, s[34:35]
	s_mov_b32 m0, s50
	s_nop 0
	global_load_lds_dwordx4 v168, vcc
	s_add_i32 m0, s50, 0x2000
	s_nop 0
	global_load_lds_dwordx4 v162, vcc
	s_waitcnt vmcnt(6)
	s_waitcnt lgkmcnt(0)
	s_barrier
	s_setprio 1
	s_waitcnt lgkmcnt(0)
	v_mfma_f32_16x16x32_bf16 v[44:47], v[130:133], v[180:183], 0
	v_mfma_f32_16x16x32_bf16 v[36:39], v[138:141], v[180:183], 0
	v_mfma_f32_16x16x32_bf16 v[28:31], v[130:133], v[188:191], 0
	v_mfma_f32_16x16x32_bf16 v[24:27], v[138:141], v[188:191], 0
	v_mfma_f32_16x16x32_bf16 v[20:23], v[130:133], v[196:199], 0
	v_mfma_f32_16x16x32_bf16 v[16:19], v[138:141], v[196:199], 0
	v_mfma_f32_16x16x32_bf16 v[12:15], v[130:133], v[204:207], 0
	v_mfma_f32_16x16x32_bf16 v[8:11], v[138:141], v[204:207], 0
	v_mfma_f32_16x16x32_bf16 v[44:47], v[134:137], v[184:187], v[44:47]
	v_mfma_f32_16x16x32_bf16 v[36:39], v[142:145], v[184:187], v[36:39]
	v_mfma_f32_16x16x32_bf16 v[28:31], v[134:137], v[192:195], v[28:31]
	v_mfma_f32_16x16x32_bf16 v[24:27], v[142:145], v[192:195], v[24:27]
	v_mfma_f32_16x16x32_bf16 v[20:23], v[134:137], v[200:203], v[20:23]
	v_mfma_f32_16x16x32_bf16 v[16:19], v[142:145], v[200:203], v[16:19]
	v_mfma_f32_16x16x32_bf16 v[12:15], v[134:137], v[208:211], v[12:15]
	v_mfma_f32_16x16x32_bf16 v[8:11], v[142:145], v[208:211], v[8:11]
	s_setprio 0
	s_setprio 1
	v_mfma_f32_16x16x32_bf16 v[4:7], v[146:149], v[180:183], 0
	v_mfma_f32_16x16x32_bf16 v[0:3], v[154:157], v[180:183], 0
	v_mfma_f32_16x16x32_bf16 v[104:107], v[146:149], v[188:191], 0
	v_mfma_f32_16x16x32_bf16 v[108:111], v[154:157], v[188:191], 0
	v_mfma_f32_16x16x32_bf16 v[112:115], v[146:149], v[196:199], 0
	v_mfma_f32_16x16x32_bf16 v[116:119], v[154:157], v[196:199], 0
	v_mfma_f32_16x16x32_bf16 v[120:123], v[146:149], v[204:207], 0
	v_mfma_f32_16x16x32_bf16 v[124:127], v[154:157], v[204:207], 0
	v_mfma_f32_16x16x32_bf16 v[4:7], v[150:153], v[184:187], v[4:7]
	v_mfma_f32_16x16x32_bf16 v[0:3], v[172:175], v[184:187], v[0:3]
	v_mfma_f32_16x16x32_bf16 v[104:107], v[150:153], v[192:195], v[104:107]
	v_mfma_f32_16x16x32_bf16 v[108:111], v[172:175], v[192:195], v[108:111]
	v_mfma_f32_16x16x32_bf16 v[112:115], v[150:153], v[200:203], v[112:115]
	v_mfma_f32_16x16x32_bf16 v[116:119], v[172:175], v[200:203], v[116:119]
	v_mfma_f32_16x16x32_bf16 v[120:123], v[150:153], v[208:211], v[120:123]
	v_mfma_f32_16x16x32_bf16 v[124:127], v[172:175], v[208:211], v[124:127]
	s_setprio 0
	s_barrier
	s_add_i32 s50, 0, 0x18000
	s_add_i32 s51, 0, 0x1c000
	v_add_u32_e32 v142, s50, v177
	v_add_u32_e32 v158, s51, v177
	ds_read_b128 v[130:133], v142
	ds_read_b128 v[134:137], v213 offset:32768
	ds_read_b128 v[138:141], v142 offset:2048
	ds_read_b128 v[142:145], v213 offset:34816
	ds_read_b128 v[146:149], v158
	ds_read_b128 v[150:153], v213 offset:49152
	ds_read_b128 v[154:157], v158 offset:2048
	ds_read_b128 v[172:175], v213 offset:51200
	s_mov_b32 m0, s29
	v_mov_b32_e32 v160, v129
	ds_read_b128 v[180:183], v178 offset:32768
	ds_read_b128 v[184:187], v212 offset:32768
	ds_read_b128 v[188:191], v178 offset:34816
	ds_read_b128 v[192:195], v212 offset:34816
	ds_read_b128 v[196:199], v178 offset:36864
	ds_read_b128 v[200:203], v212 offset:36864
	ds_read_b128 v[204:207], v178 offset:38912
	ds_read_b128 v[208:211], v212 offset:38912
	s_mov_b32 m0, s97
	s_nop 0
	global_load_lds_dwordx4 v164, s[24:25]
	s_mov_b32 m0, s28
	s_nop 0
	global_load_lds_dwordx4 v166, s[24:25]
	s_mov_b32 m0, s29
	v_mov_b32_e32 v170, v128
	global_load_lds_dwordx4 v160, s[24:25]
	s_mov_b32 m0, s30
	s_nop 0
	global_load_lds_dwordx4 v170, s[24:25]
	s_waitcnt vmcnt(8)
	s_waitcnt lgkmcnt(0)
	s_barrier
	s_setprio 1
	s_waitcnt lgkmcnt(0)
	v_mfma_f32_16x16x32_bf16 v[100:103], v[130:133], v[180:183], v[100:103]
	v_mfma_f32_16x16x32_bf16 v[96:99], v[138:141], v[180:183], v[96:99]
	v_mfma_f32_16x16x32_bf16 v[92:95], v[130:133], v[188:191], v[92:95]
	v_mfma_f32_16x16x32_bf16 v[88:91], v[138:141], v[188:191], v[88:91]
	v_mfma_f32_16x16x32_bf16 v[84:87], v[130:133], v[196:199], v[84:87]
	v_mfma_f32_16x16x32_bf16 v[80:83], v[138:141], v[196:199], v[80:83]
	v_mfma_f32_16x16x32_bf16 v[76:79], v[130:133], v[204:207], v[76:79]
	v_mfma_f32_16x16x32_bf16 v[72:75], v[138:141], v[204:207], v[72:75]
	v_mfma_f32_16x16x32_bf16 v[100:103], v[134:137], v[184:187], v[100:103]
	v_mfma_f32_16x16x32_bf16 v[96:99], v[142:145], v[184:187], v[96:99]
	v_mfma_f32_16x16x32_bf16 v[92:95], v[134:137], v[192:195], v[92:95]
	v_mfma_f32_16x16x32_bf16 v[88:91], v[142:145], v[192:195], v[88:91]
	v_mfma_f32_16x16x32_bf16 v[84:87], v[134:137], v[200:203], v[84:87]
	v_mfma_f32_16x16x32_bf16 v[80:83], v[142:145], v[200:203], v[80:83]
	v_mfma_f32_16x16x32_bf16 v[76:79], v[134:137], v[208:211], v[76:79]
	v_mfma_f32_16x16x32_bf16 v[72:75], v[142:145], v[208:211], v[72:75]
	s_setprio 0
	s_setprio 1
	v_mfma_f32_16x16x32_bf16 v[68:71], v[146:149], v[180:183], v[68:71]
	v_mfma_f32_16x16x32_bf16 v[64:67], v[154:157], v[180:183], v[64:67]
	v_mfma_f32_16x16x32_bf16 v[60:63], v[146:149], v[188:191], v[60:63]
	v_mfma_f32_16x16x32_bf16 v[56:59], v[154:157], v[188:191], v[56:59]
	v_mfma_f32_16x16x32_bf16 v[52:55], v[146:149], v[196:199], v[52:55]
	v_mfma_f32_16x16x32_bf16 v[48:51], v[154:157], v[196:199], v[48:51]
	v_mfma_f32_16x16x32_bf16 v[40:43], v[146:149], v[204:207], v[40:43]
	v_mfma_f32_16x16x32_bf16 v[32:35], v[154:157], v[204:207], v[32:35]
	v_mfma_f32_16x16x32_bf16 v[68:71], v[150:153], v[184:187], v[68:71]
	v_mfma_f32_16x16x32_bf16 v[64:67], v[172:175], v[184:187], v[64:67]
	v_mfma_f32_16x16x32_bf16 v[60:63], v[150:153], v[192:195], v[60:63]
	v_mfma_f32_16x16x32_bf16 v[56:59], v[172:175], v[192:195], v[56:59]
	v_mfma_f32_16x16x32_bf16 v[52:55], v[150:153], v[200:203], v[52:55]
	v_mfma_f32_16x16x32_bf16 v[48:51], v[172:175], v[200:203], v[48:51]
	v_mfma_f32_16x16x32_bf16 v[40:43], v[150:153], v[208:211], v[40:43]
	v_mfma_f32_16x16x32_bf16 v[32:35], v[172:175], v[208:211], v[32:35]
	s_setprio 0
	s_barrier
	v_mov_b32_e32 v169, v161
	ds_read_b128 v[180:183], v178 offset:49152
	ds_read_b128 v[184:187], v212 offset:49152
	ds_read_b128 v[188:191], v178 offset:51200
	ds_read_b128 v[192:195], v212 offset:51200
	ds_read_b128 v[196:199], v178 offset:53248
	ds_read_b128 v[200:203], v212 offset:53248
	ds_read_b128 v[204:207], v178 offset:55296
	ds_read_b128 v[208:211], v212 offset:55296
	s_add_i32 s50, s50, s61
	v_lshl_add_u64 v[128:129], s[34:35], 0, v[168:169]
	v_lshl_add_u64 v[128:129], v[128:129], 0, s[52:53]
	s_mov_b32 m0, s50
	v_mov_b32_e32 v163, v161
	global_load_lds_dwordx4 v[128:129], off
	s_add_i32 m0, s50, 0x2000
	v_mov_b32_e32 v165, v161
	v_lshl_add_u64 v[128:129], s[34:35], 0, v[162:163]
	s_add_u32 s34, s34, 0x8080
	v_lshl_add_u64 v[128:129], v[128:129], 0, s[52:53]
	s_addc_u32 s35, s35, 0
	s_add_i32 s50, s51, s61
	global_load_lds_dwordx4 v[128:129], off
	s_mov_b32 m0, s50
	v_mov_b32_e32 v167, v161
	global_load_lds_dwordx4 v168, s[34:35]
	s_add_i32 m0, s50, 0x2000
	s_nop 0
	global_load_lds_dwordx4 v162, s[34:35]
	s_mov_b32 m0, s31
	v_lshl_add_u64 v[128:129], s[24:25], 0, v[164:165]
	v_lshl_add_u64 v[128:129], v[128:129], 0, s[52:53]
	global_load_lds_dwordx4 v[128:129], off
	s_mov_b32 m0, s42
	v_lshl_add_u64 v[128:129], s[24:25], 0, v[166:167]
	v_lshl_add_u64 v[128:129], v[128:129], 0, s[52:53]
	global_load_lds_dwordx4 v[128:129], off
	s_waitcnt vmcnt(8)
	s_waitcnt lgkmcnt(0)
	s_barrier
	s_setprio 1
	s_waitcnt lgkmcnt(0)
	v_mfma_f32_16x16x32_bf16 v[44:47], v[130:133], v[180:183], v[44:47]
	v_mfma_f32_16x16x32_bf16 v[36:39], v[138:141], v[180:183], v[36:39]
	v_mfma_f32_16x16x32_bf16 v[28:31], v[130:133], v[188:191], v[28:31]
	v_mfma_f32_16x16x32_bf16 v[24:27], v[138:141], v[188:191], v[24:27]
	v_mfma_f32_16x16x32_bf16 v[20:23], v[130:133], v[196:199], v[20:23]
	v_mfma_f32_16x16x32_bf16 v[16:19], v[138:141], v[196:199], v[16:19]
	v_mfma_f32_16x16x32_bf16 v[12:15], v[130:133], v[204:207], v[12:15]
	v_mfma_f32_16x16x32_bf16 v[8:11], v[138:141], v[204:207], v[8:11]
	v_mfma_f32_16x16x32_bf16 v[44:47], v[134:137], v[184:187], v[44:47]
	v_mfma_f32_16x16x32_bf16 v[36:39], v[142:145], v[184:187], v[36:39]
	v_mfma_f32_16x16x32_bf16 v[28:31], v[134:137], v[192:195], v[28:31]
	v_mfma_f32_16x16x32_bf16 v[24:27], v[142:145], v[192:195], v[24:27]
	v_mfma_f32_16x16x32_bf16 v[20:23], v[134:137], v[200:203], v[20:23]
	v_mfma_f32_16x16x32_bf16 v[16:19], v[142:145], v[200:203], v[16:19]
	v_mfma_f32_16x16x32_bf16 v[12:15], v[134:137], v[208:211], v[12:15]
	v_mfma_f32_16x16x32_bf16 v[8:11], v[142:145], v[208:211], v[8:11]
	s_setprio 0
	s_setprio 1
	v_mfma_f32_16x16x32_bf16 v[4:7], v[146:149], v[180:183], v[4:7]
	v_mfma_f32_16x16x32_bf16 v[0:3], v[154:157], v[180:183], v[0:3]
	v_mfma_f32_16x16x32_bf16 v[104:107], v[146:149], v[188:191], v[104:107]
	v_mfma_f32_16x16x32_bf16 v[108:111], v[154:157], v[188:191], v[108:111]
	v_mfma_f32_16x16x32_bf16 v[112:115], v[146:149], v[196:199], v[112:115]
	v_mfma_f32_16x16x32_bf16 v[116:119], v[154:157], v[196:199], v[116:119]
	v_mfma_f32_16x16x32_bf16 v[120:123], v[146:149], v[204:207], v[120:123]
	v_mfma_f32_16x16x32_bf16 v[124:127], v[154:157], v[204:207], v[124:127]
	v_mfma_f32_16x16x32_bf16 v[4:7], v[150:153], v[184:187], v[4:7]
	v_mfma_f32_16x16x32_bf16 v[0:3], v[172:175], v[184:187], v[0:3]
	v_mfma_f32_16x16x32_bf16 v[104:107], v[150:153], v[192:195], v[104:107]
	v_mfma_f32_16x16x32_bf16 v[108:111], v[172:175], v[192:195], v[108:111]
	v_mfma_f32_16x16x32_bf16 v[112:115], v[150:153], v[200:203], v[112:115]
	v_mfma_f32_16x16x32_bf16 v[116:119], v[172:175], v[200:203], v[116:119]
	v_mfma_f32_16x16x32_bf16 v[120:123], v[150:153], v[208:211], v[120:123]
	v_mfma_f32_16x16x32_bf16 v[124:127], v[172:175], v[208:211], v[124:127]
	s_setprio 0
	s_barrier
	s_add_i32 s80, s80, 2
	s_add_u32 s6, s6, 0x100
	s_addc_u32 s7, s7, 0
	s_branch .LBB0_245
.LBB0_244:
	s_add_u32 vcc_lo, s70, s6
	s_addc_u32 vcc_hi, s71, s7
	s_add_u32 s81, vcc_lo, 0x32000100
	s_addc_u32 s50, vcc_hi, 0
	s_and_b64 s[24:25], s[34:35], exec
	s_cselect_b32 s25, s73, s50
	s_cselect_b32 s24, s72, s81
	s_add_u32 s50, s75, s6
	s_addc_u32 s51, s48, s7
	s_and_b64 s[34:35], s[34:35], exec
	s_cselect_b32 s35, s79, s51
	s_cselect_b32 s34, s78, s50
	s_add_i32 s50, 0, 0x10000
	s_add_i32 s51, 0, 0x14000
	v_add_u32_e32 v142, s50, v177
	v_add_u32_e32 v158, s51, v177
	ds_read_b128 v[130:133], v142
	ds_read_b128 v[134:137], v213
	ds_read_b128 v[138:141], v142 offset:2048
	ds_read_b128 v[142:145], v213 offset:2048
	ds_read_b128 v[146:149], v158
	ds_read_b128 v[150:153], v213 offset:16384
	ds_read_b128 v[154:157], v158 offset:2048
	ds_read_b128 v[172:175], v213 offset:18432
	ds_read_b128 v[180:183], v178
	ds_read_b128 v[184:187], v212
	ds_read_b128 v[188:191], v178 offset:2048
	ds_read_b128 v[192:195], v212 offset:2048
	ds_read_b128 v[196:199], v178 offset:4096
	ds_read_b128 v[200:203], v212 offset:4096
	ds_read_b128 v[204:207], v178 offset:6144
	ds_read_b128 v[208:211], v212 offset:6144
	s_add_i32 m0, s97, 0xc000
	v_lshl_add_u64 v[158:159], vcc, 0, v[160:161]
	v_lshl_add_u64 v[158:159], v[158:159], 0, s[54:55]
	v_mov_b32_e32 v171, v161
	global_load_lds_dwordx4 v[158:159], off
	s_add_i32 m0, s97, 0xe000
	v_lshl_add_u64 v[158:159], vcc, 0, v[170:171]
	v_lshl_add_u64 v[158:159], v[158:159], 0, s[54:55]
	global_load_lds_dwordx4 v[158:159], off
	s_waitcnt vmcnt(8)
	s_waitcnt lgkmcnt(0)
	s_barrier
	s_setprio 1
	s_waitcnt lgkmcnt(0)
	v_mfma_f32_16x16x32_bf16 v[100:103], v[130:133], v[180:183], v[100:103]
	v_mfma_f32_16x16x32_bf16 v[96:99], v[138:141], v[180:183], v[96:99]
	v_mfma_f32_16x16x32_bf16 v[92:95], v[130:133], v[188:191], v[92:95]
	v_mfma_f32_16x16x32_bf16 v[88:91], v[138:141], v[188:191], v[88:91]
	v_mfma_f32_16x16x32_bf16 v[84:87], v[130:133], v[196:199], v[84:87]
	v_mfma_f32_16x16x32_bf16 v[80:83], v[138:141], v[196:199], v[80:83]
	v_mfma_f32_16x16x32_bf16 v[76:79], v[130:133], v[204:207], v[76:79]
	v_mfma_f32_16x16x32_bf16 v[72:75], v[138:141], v[204:207], v[72:75]
	v_mfma_f32_16x16x32_bf16 v[100:103], v[134:137], v[184:187], v[100:103]
	v_mfma_f32_16x16x32_bf16 v[96:99], v[142:145], v[184:187], v[96:99]
	v_mfma_f32_16x16x32_bf16 v[92:95], v[134:137], v[192:195], v[92:95]
	v_mfma_f32_16x16x32_bf16 v[88:91], v[142:145], v[192:195], v[88:91]
	v_mfma_f32_16x16x32_bf16 v[84:87], v[134:137], v[200:203], v[84:87]
	v_mfma_f32_16x16x32_bf16 v[80:83], v[142:145], v[200:203], v[80:83]
	v_mfma_f32_16x16x32_bf16 v[76:79], v[134:137], v[208:211], v[76:79]
	v_mfma_f32_16x16x32_bf16 v[72:75], v[142:145], v[208:211], v[72:75]
	s_setprio 0
	s_setprio 1
	v_mfma_f32_16x16x32_bf16 v[68:71], v[146:149], v[180:183], v[68:71]
	v_mfma_f32_16x16x32_bf16 v[64:67], v[154:157], v[180:183], v[64:67]
	v_mfma_f32_16x16x32_bf16 v[60:63], v[146:149], v[188:191], v[60:63]
	v_mfma_f32_16x16x32_bf16 v[56:59], v[154:157], v[188:191], v[56:59]
	v_mfma_f32_16x16x32_bf16 v[52:55], v[146:149], v[196:199], v[52:55]
	v_mfma_f32_16x16x32_bf16 v[48:51], v[154:157], v[196:199], v[48:51]
	v_mfma_f32_16x16x32_bf16 v[40:43], v[146:149], v[204:207], v[40:43]
	v_mfma_f32_16x16x32_bf16 v[32:35], v[154:157], v[204:207], v[32:35]
	v_mfma_f32_16x16x32_bf16 v[68:71], v[150:153], v[184:187], v[68:71]
	v_mfma_f32_16x16x32_bf16 v[64:67], v[172:175], v[184:187], v[64:67]
	v_mfma_f32_16x16x32_bf16 v[60:63], v[150:153], v[192:195], v[60:63]
	v_mfma_f32_16x16x32_bf16 v[56:59], v[172:175], v[192:195], v[56:59]
	v_mfma_f32_16x16x32_bf16 v[52:55], v[150:153], v[200:203], v[52:55]
	v_mfma_f32_16x16x32_bf16 v[48:51], v[172:175], v[200:203], v[48:51]
	v_mfma_f32_16x16x32_bf16 v[40:43], v[150:153], v[208:211], v[40:43]
	v_mfma_f32_16x16x32_bf16 v[32:35], v[172:175], v[208:211], v[32:35]
	s_setprio 0
	s_barrier
	s_add_i32 s50, s50, s61
	s_mov_b32 m0, s50
	ds_read_b128 v[180:183], v178 offset:16384
	ds_read_b128 v[184:187], v212 offset:16384
	ds_read_b128 v[188:191], v178 offset:18432
	ds_read_b128 v[192:195], v212 offset:18432
	ds_read_b128 v[196:199], v178 offset:20480
	ds_read_b128 v[200:203], v212 offset:20480
	ds_read_b128 v[204:207], v178 offset:22528
	ds_read_b128 v[208:211], v212 offset:22528
	s_nop 0
	global_load_lds_dwordx4 v168, s[34:35]
	s_add_i32 m0, s50, 0x2000
	s_add_u32 vcc_lo, s34, 0x8000
	s_addc_u32 vcc_hi, s35, 0
	s_add_i32 s50, s51, s61
	s_nop 0
	global_load_lds_dwordx4 v162, s[34:35]
	s_mov_b32 m0, s50
	s_nop 0
	global_load_lds_dwordx4 v168, vcc
	s_add_i32 m0, s50, 0x2000
	s_nop 0
	global_load_lds_dwordx4 v162, vcc
	s_waitcnt vmcnt(6)
	s_waitcnt lgkmcnt(0)
	s_barrier
	s_setprio 1
	s_waitcnt lgkmcnt(0)
	v_mfma_f32_16x16x32_bf16 v[44:47], v[130:133], v[180:183], v[44:47]
	v_mfma_f32_16x16x32_bf16 v[36:39], v[138:141], v[180:183], v[36:39]
	v_mfma_f32_16x16x32_bf16 v[28:31], v[130:133], v[188:191], v[28:31]
	v_mfma_f32_16x16x32_bf16 v[24:27], v[138:141], v[188:191], v[24:27]
	v_mfma_f32_16x16x32_bf16 v[20:23], v[130:133], v[196:199], v[20:23]
	v_mfma_f32_16x16x32_bf16 v[16:19], v[138:141], v[196:199], v[16:19]
	v_mfma_f32_16x16x32_bf16 v[12:15], v[130:133], v[204:207], v[12:15]
	v_mfma_f32_16x16x32_bf16 v[8:11], v[138:141], v[204:207], v[8:11]
	v_mfma_f32_16x16x32_bf16 v[44:47], v[134:137], v[184:187], v[44:47]
	v_mfma_f32_16x16x32_bf16 v[36:39], v[142:145], v[184:187], v[36:39]
	v_mfma_f32_16x16x32_bf16 v[28:31], v[134:137], v[192:195], v[28:31]
	v_mfma_f32_16x16x32_bf16 v[24:27], v[142:145], v[192:195], v[24:27]
	v_mfma_f32_16x16x32_bf16 v[20:23], v[134:137], v[200:203], v[20:23]
	v_mfma_f32_16x16x32_bf16 v[16:19], v[142:145], v[200:203], v[16:19]
	v_mfma_f32_16x16x32_bf16 v[12:15], v[134:137], v[208:211], v[12:15]
	v_mfma_f32_16x16x32_bf16 v[8:11], v[142:145], v[208:211], v[8:11]
	s_setprio 0
	s_setprio 1
	v_mfma_f32_16x16x32_bf16 v[4:7], v[146:149], v[180:183], v[4:7]
	v_mfma_f32_16x16x32_bf16 v[0:3], v[154:157], v[180:183], v[0:3]
	v_mfma_f32_16x16x32_bf16 v[104:107], v[146:149], v[188:191], v[104:107]
	v_mfma_f32_16x16x32_bf16 v[108:111], v[154:157], v[188:191], v[108:111]
	v_mfma_f32_16x16x32_bf16 v[112:115], v[146:149], v[196:199], v[112:115]
	v_mfma_f32_16x16x32_bf16 v[116:119], v[154:157], v[196:199], v[116:119]
	v_mfma_f32_16x16x32_bf16 v[120:123], v[146:149], v[204:207], v[120:123]
	v_mfma_f32_16x16x32_bf16 v[124:127], v[154:157], v[204:207], v[124:127]
	v_mfma_f32_16x16x32_bf16 v[4:7], v[150:153], v[184:187], v[4:7]
	v_mfma_f32_16x16x32_bf16 v[0:3], v[172:175], v[184:187], v[0:3]
	v_mfma_f32_16x16x32_bf16 v[104:107], v[150:153], v[192:195], v[104:107]
	v_mfma_f32_16x16x32_bf16 v[108:111], v[172:175], v[192:195], v[108:111]
	v_mfma_f32_16x16x32_bf16 v[112:115], v[150:153], v[200:203], v[112:115]
	v_mfma_f32_16x16x32_bf16 v[116:119], v[172:175], v[200:203], v[116:119]
	v_mfma_f32_16x16x32_bf16 v[120:123], v[150:153], v[208:211], v[120:123]
	v_mfma_f32_16x16x32_bf16 v[124:127], v[172:175], v[208:211], v[124:127]
	s_setprio 0
	s_barrier
	s_add_i32 s50, 0, 0x18000
	s_add_i32 s51, 0, 0x1c000
	v_add_u32_e32 v142, s50, v177
	v_add_u32_e32 v158, s51, v177
	ds_read_b128 v[130:133], v142
	ds_read_b128 v[134:137], v213 offset:32768
	ds_read_b128 v[138:141], v142 offset:2048
	ds_read_b128 v[142:145], v213 offset:34816
	ds_read_b128 v[146:149], v158
	ds_read_b128 v[150:153], v213 offset:49152
	ds_read_b128 v[154:157], v158 offset:2048
	ds_read_b128 v[172:175], v213 offset:51200
	s_mov_b32 m0, s29
	v_mov_b32_e32 v160, v129
	ds_read_b128 v[180:183], v178 offset:32768
	ds_read_b128 v[184:187], v212 offset:32768
	ds_read_b128 v[188:191], v178 offset:34816
	ds_read_b128 v[192:195], v212 offset:34816
	ds_read_b128 v[196:199], v178 offset:36864
	ds_read_b128 v[200:203], v212 offset:36864
	ds_read_b128 v[204:207], v178 offset:38912
	ds_read_b128 v[208:211], v212 offset:38912
	s_mov_b32 m0, s97
	s_nop 0
	global_load_lds_dwordx4 v164, s[24:25]
	s_mov_b32 m0, s28
	s_nop 0
	global_load_lds_dwordx4 v166, s[24:25]
	s_mov_b32 m0, s29
	v_mov_b32_e32 v170, v128
	global_load_lds_dwordx4 v160, s[24:25]
	s_mov_b32 m0, s30
	s_nop 0
	global_load_lds_dwordx4 v170, s[24:25]
	s_waitcnt vmcnt(8)
	s_waitcnt lgkmcnt(0)
	s_barrier
	s_setprio 1
	s_waitcnt lgkmcnt(0)
	v_mfma_f32_16x16x32_bf16 v[100:103], v[130:133], v[180:183], v[100:103]
	v_mfma_f32_16x16x32_bf16 v[96:99], v[138:141], v[180:183], v[96:99]
	v_mfma_f32_16x16x32_bf16 v[92:95], v[130:133], v[188:191], v[92:95]
	v_mfma_f32_16x16x32_bf16 v[88:91], v[138:141], v[188:191], v[88:91]
	v_mfma_f32_16x16x32_bf16 v[84:87], v[130:133], v[196:199], v[84:87]
	v_mfma_f32_16x16x32_bf16 v[80:83], v[138:141], v[196:199], v[80:83]
	v_mfma_f32_16x16x32_bf16 v[76:79], v[130:133], v[204:207], v[76:79]
	v_mfma_f32_16x16x32_bf16 v[72:75], v[138:141], v[204:207], v[72:75]
	v_mfma_f32_16x16x32_bf16 v[100:103], v[134:137], v[184:187], v[100:103]
	v_mfma_f32_16x16x32_bf16 v[96:99], v[142:145], v[184:187], v[96:99]
	v_mfma_f32_16x16x32_bf16 v[92:95], v[134:137], v[192:195], v[92:95]
	v_mfma_f32_16x16x32_bf16 v[88:91], v[142:145], v[192:195], v[88:91]
	v_mfma_f32_16x16x32_bf16 v[84:87], v[134:137], v[200:203], v[84:87]
	v_mfma_f32_16x16x32_bf16 v[80:83], v[142:145], v[200:203], v[80:83]
	v_mfma_f32_16x16x32_bf16 v[76:79], v[134:137], v[208:211], v[76:79]
	v_mfma_f32_16x16x32_bf16 v[72:75], v[142:145], v[208:211], v[72:75]
	s_setprio 0
	s_setprio 1
	v_mfma_f32_16x16x32_bf16 v[68:71], v[146:149], v[180:183], v[68:71]
	v_mfma_f32_16x16x32_bf16 v[64:67], v[154:157], v[180:183], v[64:67]
	v_mfma_f32_16x16x32_bf16 v[60:63], v[146:149], v[188:191], v[60:63]
	v_mfma_f32_16x16x32_bf16 v[56:59], v[154:157], v[188:191], v[56:59]
	v_mfma_f32_16x16x32_bf16 v[52:55], v[146:149], v[196:199], v[52:55]
	v_mfma_f32_16x16x32_bf16 v[48:51], v[154:157], v[196:199], v[48:51]
	v_mfma_f32_16x16x32_bf16 v[40:43], v[146:149], v[204:207], v[40:43]
	v_mfma_f32_16x16x32_bf16 v[32:35], v[154:157], v[204:207], v[32:35]
	v_mfma_f32_16x16x32_bf16 v[68:71], v[150:153], v[184:187], v[68:71]
	v_mfma_f32_16x16x32_bf16 v[64:67], v[172:175], v[184:187], v[64:67]
	v_mfma_f32_16x16x32_bf16 v[60:63], v[150:153], v[192:195], v[60:63]
	v_mfma_f32_16x16x32_bf16 v[56:59], v[172:175], v[192:195], v[56:59]
	v_mfma_f32_16x16x32_bf16 v[52:55], v[150:153], v[200:203], v[52:55]
	v_mfma_f32_16x16x32_bf16 v[48:51], v[172:175], v[200:203], v[48:51]
	v_mfma_f32_16x16x32_bf16 v[40:43], v[150:153], v[208:211], v[40:43]
	v_mfma_f32_16x16x32_bf16 v[32:35], v[172:175], v[208:211], v[32:35]
	s_setprio 0
	s_barrier
	v_mov_b32_e32 v169, v161
	ds_read_b128 v[180:183], v178 offset:49152
	ds_read_b128 v[184:187], v212 offset:49152
	ds_read_b128 v[188:191], v178 offset:51200
	ds_read_b128 v[192:195], v212 offset:51200
	ds_read_b128 v[196:199], v178 offset:53248
	ds_read_b128 v[200:203], v212 offset:53248
	ds_read_b128 v[204:207], v178 offset:55296
	ds_read_b128 v[208:211], v212 offset:55296
	s_add_i32 s50, s50, s61
	v_lshl_add_u64 v[128:129], s[34:35], 0, v[168:169]
	v_lshl_add_u64 v[128:129], v[128:129], 0, s[52:53]
	s_mov_b32 m0, s50
	v_mov_b32_e32 v163, v161
	global_load_lds_dwordx4 v[128:129], off
	s_add_i32 m0, s50, 0x2000
	v_mov_b32_e32 v165, v161
	v_lshl_add_u64 v[128:129], s[34:35], 0, v[162:163]
	s_add_u32 s34, s34, 0x8080
	v_lshl_add_u64 v[128:129], v[128:129], 0, s[52:53]
	s_addc_u32 s35, s35, 0
	s_add_i32 s50, s51, s61
	global_load_lds_dwordx4 v[128:129], off
	s_mov_b32 m0, s50
	v_mov_b32_e32 v167, v161
	global_load_lds_dwordx4 v168, s[34:35]
	s_add_i32 m0, s50, 0x2000
	s_nop 0
	global_load_lds_dwordx4 v162, s[34:35]
	s_mov_b32 m0, s31
	v_lshl_add_u64 v[128:129], s[24:25], 0, v[164:165]
	v_lshl_add_u64 v[128:129], v[128:129], 0, s[52:53]
	global_load_lds_dwordx4 v[128:129], off
	s_mov_b32 m0, s42
	v_lshl_add_u64 v[128:129], s[24:25], 0, v[166:167]
	v_lshl_add_u64 v[128:129], v[128:129], 0, s[52:53]
	global_load_lds_dwordx4 v[128:129], off
	s_waitcnt vmcnt(8)
	s_waitcnt lgkmcnt(0)
	s_barrier
	s_setprio 1
	s_waitcnt lgkmcnt(0)
	v_mfma_f32_16x16x32_bf16 v[44:47], v[130:133], v[180:183], v[44:47]
	v_mfma_f32_16x16x32_bf16 v[36:39], v[138:141], v[180:183], v[36:39]
	v_mfma_f32_16x16x32_bf16 v[28:31], v[130:133], v[188:191], v[28:31]
	v_mfma_f32_16x16x32_bf16 v[24:27], v[138:141], v[188:191], v[24:27]
	v_mfma_f32_16x16x32_bf16 v[20:23], v[130:133], v[196:199], v[20:23]
	v_mfma_f32_16x16x32_bf16 v[16:19], v[138:141], v[196:199], v[16:19]
	v_mfma_f32_16x16x32_bf16 v[12:15], v[130:133], v[204:207], v[12:15]
	v_mfma_f32_16x16x32_bf16 v[8:11], v[138:141], v[204:207], v[8:11]
	v_mfma_f32_16x16x32_bf16 v[44:47], v[134:137], v[184:187], v[44:47]
	v_mfma_f32_16x16x32_bf16 v[36:39], v[142:145], v[184:187], v[36:39]
	v_mfma_f32_16x16x32_bf16 v[28:31], v[134:137], v[192:195], v[28:31]
	v_mfma_f32_16x16x32_bf16 v[24:27], v[142:145], v[192:195], v[24:27]
	v_mfma_f32_16x16x32_bf16 v[20:23], v[134:137], v[200:203], v[20:23]
	v_mfma_f32_16x16x32_bf16 v[16:19], v[142:145], v[200:203], v[16:19]
	v_mfma_f32_16x16x32_bf16 v[12:15], v[134:137], v[208:211], v[12:15]
	v_mfma_f32_16x16x32_bf16 v[8:11], v[142:145], v[208:211], v[8:11]
	s_setprio 0
	s_setprio 1
	v_mfma_f32_16x16x32_bf16 v[4:7], v[146:149], v[180:183], v[4:7]
	v_mfma_f32_16x16x32_bf16 v[0:3], v[154:157], v[180:183], v[0:3]
	v_mfma_f32_16x16x32_bf16 v[104:107], v[146:149], v[188:191], v[104:107]
	v_mfma_f32_16x16x32_bf16 v[108:111], v[154:157], v[188:191], v[108:111]
	v_mfma_f32_16x16x32_bf16 v[112:115], v[146:149], v[196:199], v[112:115]
	v_mfma_f32_16x16x32_bf16 v[116:119], v[154:157], v[196:199], v[116:119]
	v_mfma_f32_16x16x32_bf16 v[120:123], v[146:149], v[204:207], v[120:123]
	v_mfma_f32_16x16x32_bf16 v[124:127], v[154:157], v[204:207], v[124:127]
	v_mfma_f32_16x16x32_bf16 v[4:7], v[150:153], v[184:187], v[4:7]
	v_mfma_f32_16x16x32_bf16 v[0:3], v[172:175], v[184:187], v[0:3]
	v_mfma_f32_16x16x32_bf16 v[104:107], v[150:153], v[192:195], v[104:107]
	v_mfma_f32_16x16x32_bf16 v[108:111], v[172:175], v[192:195], v[108:111]
	v_mfma_f32_16x16x32_bf16 v[112:115], v[150:153], v[200:203], v[112:115]
	v_mfma_f32_16x16x32_bf16 v[116:119], v[172:175], v[200:203], v[116:119]
	v_mfma_f32_16x16x32_bf16 v[120:123], v[150:153], v[208:211], v[120:123]
	v_mfma_f32_16x16x32_bf16 v[124:127], v[172:175], v[208:211], v[124:127]
	s_setprio 0
	s_barrier
	s_add_i32 s80, s80, 2
	s_add_u32 s6, s6, 0x100
	s_addc_u32 s7, s7, 0
	s_cmp_gt_u32 s80, 29
	s_cbranch_scc1 .LBB0_247
.LBB0_245:
	s_cmp_eq_u32 s80, 28
	s_cselect_b64 s[34:35], -1, 0
	s_and_b64 s[24:25], s[0:1], s[34:35]
	s_andn2_b64 vcc, exec, s[24:25]
	v_mov_b32_e32 v128, v170
	v_mov_b32_e32 v129, v160
	s_cbranch_vccnz .LBB0_244
	v_mbcnt_lo_u32_b32 v128, -1, 0
	v_mbcnt_hi_u32_b32 v128, -1, v128
	v_and_b32_e32 v130, 7, v128
	v_add_u32_e32 v128, s33, v128
	v_lshrrev_b32_e32 v131, 3, v128
	v_bfe_u32 v128, v131, 1, 3
	v_and_b32_e32 v129, 1, v128
	v_lshlrev_b32_e32 v129, 1, v129
	v_and_or_b32 v128, v128, 4, v129
	v_xor_b32_e32 v130, v130, v128
	v_lshlrev_b32_e32 v130, 4, v130
	v_add_u32_e32 v132, 64, v131
	v_lshlrev_b32_e32 v129, 12, v131
	v_add3_u32 v164, v129, s8, v130
	v_lshlrev_b32_e32 v129, 12, v132
	v_add3_u32 v166, v129, s8, v130
	v_add_u32_e32 v129, s49, v131
	v_lshl_add_u32 v129, v129, 12, v130
	v_add_u32_e32 v128, s49, v132
	v_lshl_add_u32 v128, v128, 12, v130
	s_branch .LBB0_244

.LBB0_621:
	v_add_u32_e32 v1, s33, v2
	v_ashrrev_i32_e32 v4, 31, v1
	v_lshrrev_b32_e32 v4, 26, v4
	v_lshlrev_b32_e32 v3, 4, v1
	v_add_u32_e32 v4, v1, v4
	v_bfe_i32 v1, v1, 27, 1
	v_lshrrev_b32_e32 v1, 22, v1
	v_add_u32_e32 v1, v3, v1
	v_and_b32_e32 v1, 0xfffffc00, v1
	v_sub_u32_e32 v1, v3, v1
	v_lshrrev_b32_e32 v5, 4, v1
	v_bitop3_b32 v1, v5, v1, 32 bitop3:0x6c
	v_ashrrev_i32_e32 v6, 31, v1
	v_lshrrev_b32_e32 v6, 26, v6
	v_ashrrev_i32_e32 v4, 6, v4
	v_add_u32_e32 v6, v1, v6
	v_lshlrev_b32_e32 v5, 3, v4
	v_ashrrev_i32_e32 v7, 6, v6
	v_and_b32_e32 v6, 0xc0, v6
	v_and_b32_e32 v5, -16, v5
	v_lshlrev_b32_e32 v4, 5, v4
	v_sub_u32_e32 v1, v1, v6
	v_mov_b32_e32 v174, 1
	v_add_u32_e32 v5, v7, v5
	v_and_b32_e32 v4, 32, v4
	v_ashrrev_i16_sdwa v1, v174, sext(v1) dst_sel:DWORD dst_unused:UNUSED_PAD src0_sel:DWORD src1_sel:BYTE_0
	v_add_u32_sdwa v1, v4, sext(v1) dst_sel:DWORD dst_unused:UNUSED_PAD src0_sel:DWORD src1_sel:WORD_0
	v_and_b32_e32 v4, 0x7ffe0, v5
	v_lshlrev_b32_e32 v6, 1, v5
	v_lshrrev_b32_e32 v5, 2, v5
	v_and_b32_e32 v7, 3, v7
	v_and_or_b32 v5, v5, 4, v7
	v_and_or_b32 v4, v6, 24, v4
	v_lshlrev_b32_e32 v5, 12, v5
	v_lshl_or_b32 v4, v4, 13, v5
	v_lshl_add_u32 v156, v1, 1, v4
	v_add_u32_e32 v1, 0x2000, v3
	v_ashrrev_i32_e32 v3, 31, v1
	v_lshrrev_b32_e32 v3, 22, v3
	v_add_u32_e32 v3, v1, v3
	v_ashrrev_i32_e32 v3, 10, v3
	v_mul_i32_i24_e32 v4, 0x400, v3
	v_sub_u32_e32 v1, v1, v4
	v_lshrrev_b32_e32 v4, 4, v1
	v_bitop3_b32 v1, v4, v1, 32 bitop3:0x6c
	v_ashrrev_i32_e32 v5, 31, v1
	v_lshrrev_b32_e32 v5, 26, v5
	v_add_u32_e32 v5, v1, v5
	v_lshlrev_b32_e32 v4, 3, v3
	v_ashrrev_i32_e32 v6, 6, v5
	v_and_b32_e32 v5, 0xc0, v5
	v_and_b32_e32 v4, -16, v4
	v_lshlrev_b32_e32 v3, 5, v3
	v_sub_u32_e32 v1, v1, v5
	v_add_u32_e32 v4, v6, v4
	v_and_b32_e32 v3, 32, v3
	v_ashrrev_i16_sdwa v1, v174, sext(v1) dst_sel:DWORD dst_unused:UNUSED_PAD src0_sel:DWORD src1_sel:BYTE_0
	v_add_u32_sdwa v1, v3, sext(v1) dst_sel:DWORD dst_unused:UNUSED_PAD src0_sel:DWORD src1_sel:WORD_0
	v_and_b32_e32 v3, 0x7ffe0, v4
	v_lshlrev_b32_e32 v5, 1, v4
	v_lshrrev_b32_e32 v4, 2, v4
	v_and_b32_e32 v6, 3, v6
	v_and_or_b32 v4, v4, 4, v6
	v_and_or_b32 v3, v5, 24, v3
	v_lshlrev_b32_e32 v4, 12, v4
	v_lshl_or_b32 v3, v3, 13, v4
	v_lshl_add_u32 v158, v1, 1, v3
	v_add_u32_e32 v1, s33, v2
	v_lshrrev_b32_e32 v3, 3, v1
	v_and_b32_e32 v1, 7, v1
	v_bfe_u32 v4, v3, 1, 3
	v_and_b32_e32 v5, 1, v4
	v_lshlrev_b32_e32 v5, 1, v5
	v_and_or_b32 v4, v4, 4, v5
	v_xor_b32_e32 v1, v1, v4
	v_lshlrev_b32_e32 v1, 4, v1
	v_lshrrev_b32_e32 v4, 5, v3
	v_lshlrev_b32_e32 v4, 6, v4
	v_bfe_u32 v5, v3, 2, 2
	v_lshl_or_b32 v4, v5, 4, v4
	v_bfe_u32 v5, v3, 4, 1
	v_lshl_or_b32 v4, v5, 2, v4
	v_and_b32_e32 v5, 3, v3
	v_or_b32_e32 v4, v4, v5
	v_lshl_add_u32 v156, v4, 12, v1
	v_add_u32_e32 v158, 0x80000, v156
	s_waitcnt lgkmcnt(0)
	s_barrier
	v_mbcnt_lo_u32_b32 v1, -1, 0
	v_mbcnt_hi_u32_b32 v1, -1, v1
	s_waitcnt lgkmcnt(0)
	s_add_u32 s12, s6, 0x46000000
	v_add_u32_e32 v1, s33, v1
	v_ashrrev_i32_e32 v4, 31, v1
	v_lshrrev_b32_e32 v4, 26, v4
	v_lshlrev_b32_e32 v3, 4, v1
	v_add_u32_e32 v4, v1, v4
	v_bfe_i32 v1, v1, 27, 1
	v_lshrrev_b32_e32 v1, 22, v1
	v_add_u32_e32 v1, v3, v1
	v_and_b32_e32 v1, 0xfffffc00, v1
	v_sub_u32_e32 v1, v3, v1
	v_lshrrev_b32_e32 v5, 4, v1
	v_bitop3_b32 v1, v5, v1, 32 bitop3:0x6c
	v_ashrrev_i32_e32 v6, 31, v1
	v_lshrrev_b32_e32 v6, 26, v6
	v_add_u32_e32 v6, v1, v6
	v_ashrrev_i32_e32 v7, 6, v6
	v_and_b32_e32 v6, 0xc0, v6
	v_ashrrev_i32_e32 v4, 6, v4
	v_sub_u32_e32 v1, v1, v6
	v_lshlrev_b32_e32 v5, 3, v4
	v_lshlrev_b32_e32 v4, 5, v4
	v_ashrrev_i16_sdwa v1, v174, sext(v1) dst_sel:DWORD dst_unused:UNUSED_PAD src0_sel:DWORD src1_sel:BYTE_0
	v_and_b32_e32 v4, 32, v4
	v_bfe_i32 v1, v1, 0, 16
	v_add_u32_e32 v3, 0x2000, v3
	v_add_lshl_u32 v1, v4, v1, 1
	v_ashrrev_i32_e32 v4, 31, v3
	v_lshrrev_b32_e32 v4, 22, v4
	s_addc_u32 s13, s7, 0
	s_ashr_i32 s11, s10, 31
	v_add_u32_e32 v4, v3, v4
	s_lshl_b64 s[14:15], s[10:11], 20
	v_ashrrev_i32_e32 v4, 10, v4
	s_add_u32 s2, s2, s14
	v_mul_i32_i24_e32 v6, 0x400, v4
	s_addc_u32 s3, s3, s15
	v_sub_u32_e32 v3, v3, v6
	s_add_u32 s36, s2, 0x1000000
	v_lshrrev_b32_e32 v6, 4, v3
	s_addc_u32 s37, s3, 0
	s_lshr_b32 s9, s61, 8
	v_and_b32_e32 v5, -16, v5
	v_bitop3_b32 v3, v6, v3, 32 bitop3:0x6c
	s_cmp_eq_u32 s9, 1
	v_add_u32_e32 v5, v7, v5
	v_ashrrev_i32_e32 v7, 31, v3
	s_cselect_b64 s[14:15], -1, 0
	s_lshl_b32 s11, s8, 8
	v_lshrrev_b32_e32 v7, 26, v7
	s_or_b32 s17, s11, 0x80
	s_add_i32 s11, s42, 0
	v_add_u32_e32 v7, v3, v7
	s_lshl_b32 s16, s8, 20
	s_add_i32 m0, s11, 0x10000
	s_add_i32 s18, s11, 0x12000
	v_ashrrev_i32_e32 v8, 6, v7
	v_and_b32_e32 v7, 0xc0, v7
	s_add_u32 s2, s2, 0x1008000
	v_sub_u32_e32 v3, v3, v7
	s_addc_u32 s3, s3, 0
	s_add_i32 s19, s11, 0x14000
	v_lshlrev_b32_e32 v6, 3, v4
	v_lshlrev_b32_e32 v4, 5, v4
	v_ashrrev_i16_sdwa v3, v174, sext(v3) dst_sel:DWORD dst_unused:UNUSED_PAD src0_sel:DWORD src1_sel:BYTE_0
	s_add_i32 s20, s11, 0x16000
	global_load_lds_dwordx4 v156, s[36:37]
	s_mov_b32 m0, s18
	v_and_b32_e32 v6, -16, v6
	v_and_b32_e32 v4, 32, v4
	v_bfe_i32 v3, v3, 0, 16
	v_add_u32_e32 v6, v8, v6
	global_load_lds_dwordx4 v158, s[36:37]
	s_mov_b32 m0, s19
	v_add_lshl_u32 v3, v4, v3, 1
	v_add_u32_e32 v7, s33, v2
	v_lshrrev_b32_e32 v5, 3, v7
	v_add_u32_e32 v6, 64, v5
	v_and_b32_e32 v1, 7, v2
	v_bfe_u32 v7, v5, 1, 3
	v_and_b32_e32 v8, 1, v7
	v_lshlrev_b32_e32 v8, 1, v8
	v_and_or_b32 v7, v7, 4, v8
	v_xor_b32_e32 v1, v1, v7
	v_lshlrev_b32_e32 v1, 4, v1
	v_mov_b32_e32 v3, v1
	v_lshlrev_b32_e32 v4, 12, v5
	s_add_i32 s44, s11, 0x2000
	global_load_lds_dwordx4 v156, s[2:3]
	s_mov_b32 m0, s20
	v_add3_u32 v160, v4, s16, v1
	v_lshlrev_b32_e32 v4, 12, v6
	s_add_i32 s45, s11, 0x4000
	global_load_lds_dwordx4 v158, s[2:3]
	s_mov_b32 m0, s11
	v_add3_u32 v162, v4, s16, v3
	v_add_u32_e32 v4, s17, v5
	s_add_i32 s46, s11, 0x6000
	global_load_lds_dwordx4 v160, s[12:13]
	s_mov_b32 m0, s44
	v_lshl_add_u32 v104, v4, 12, v1
	v_add_u32_e32 v1, s17, v6
	v_lshl_add_u32 v166, v1, 12, v3
	global_load_lds_dwordx4 v162, s[12:13]
	s_mov_b32 m0, s45
	s_cmp_lg_u32 s9, 1
	global_load_lds_dwordx4 v104, s[12:13]
	s_mov_b32 m0, s46
	s_nop 0
	global_load_lds_dwordx4 v166, s[12:13]
	s_cbranch_scc1 .LBB0_623
	s_barrier
.LBB0_623:
	s_bfe_u32 s20, s61, 0x20006
	s_lshl_b32 s47, s9, 6
	v_mov_b32_e32 v157, 0
	s_cmpk_lt_u32 s61, 0x100
	s_waitcnt vmcnt(2)
	s_barrier
	s_mov_b64 s[18:19], 0x80
	v_lshl_add_u64 v[4:5], s[36:37], 0, v[156:157]
	s_cselect_b64 s[16:17], -1, 0
	v_lshl_add_u64 v[4:5], v[4:5], 0, s[18:19]
	s_add_i32 m0, s11, 0x18000
	s_lshl_b32 s48, s20, 6
	global_load_lds_dwordx4 v[4:5], off
	v_mov_b32_e32 v159, v157
	s_add_i32 m0, s11, 0x1a000
	s_add_u32 s2, s6, 0x46000080
	v_lshl_add_u64 v[4:5], s[36:37], 0, v[158:159]
	v_lshl_add_u64 v[4:5], v[4:5], 0, s[18:19]
	s_addc_u32 s3, s7, 0
	s_add_i32 s49, s11, 0x8000
	global_load_lds_dwordx4 v[4:5], off
	s_mov_b32 m0, s49
	s_add_i32 s50, s11, 0xa000
	v_and_b32_e32 v1, 48, v2
	global_load_lds_dwordx4 v160, s[2:3]
	s_mov_b32 m0, s50
	v_and_b32_e32 v0, 0xfffffc00, v0
	global_load_lds_dwordx4 v162, s[2:3]
	s_add_u32 s2, s36, 0x8080
	s_addc_u32 s3, s37, 0
	s_add_i32 m0, s11, 0x1c000
	v_lshlrev_b32_e32 v4, 6, v2
	global_load_lds_dwordx4 v156, s[2:3]
	s_add_i32 m0, s11, 0x1e000
	v_lshlrev_b32_e32 v2, 2, v2
	global_load_lds_dwordx4 v158, s[2:3]
	s_movk_i32 s2, 0x3c0
	v_lshl_add_u32 v3, s9, 13, v0
	v_and_or_b32 v1, v4, s2, v1
	v_and_b32_e32 v2, 32, v2
	v_lshl_add_u32 v0, s20, 12, v0
	v_bitop3_b32 v4, v1, v3, v2 bitop3:0xde
	v_bitop3_b32 v175, v1, v0, v2 bitop3:0xde
	v_mbcnt_lo_u32_b32 v0, -1, 0
	v_mbcnt_hi_u32_b32 v0, -1, v0
	v_and_b32_e32 v1, 15, v0
	v_lshrrev_b32_e32 v0, 4, v0
	v_bfe_u32 v2, v1, 1, 3
	v_and_b32_e32 v3, 1, v2
	v_lshlrev_b32_e32 v3, 1, v3
	v_and_or_b32 v2, v2, 4, v3
	v_xor_b32_e32 v0, v0, v2
	v_lshlrev_b32_e32 v0, 4, v0
	v_lshl_add_u32 v0, v1, 7, v0
	v_lshl_add_u32 v4, s9, 13, v0
	v_xor_b32_e32 v177, 64, v4
	v_lshl_add_u32 v175, s20, 12, v0
	s_waitcnt vmcnt(6)
	v_mov_b32_e32 v2, v157
	v_mov_b32_e32 v3, v157
	v_mov_b32_e32 v164, v156
	v_mov_b32_e32 v0, v157
	v_mov_b32_e32 v1, v157
	v_add_u32_e32 v176, 0, v4
	v_mov_b64_e32 v[18:19], v[2:3]
	v_mov_b64_e32 v[26:27], v[2:3]
	v_mov_b64_e32 v[34:35], v[2:3]
	v_mov_b64_e32 v[42:43], v[2:3]
	v_mov_b64_e32 v[50:51], v[2:3]
	v_mov_b64_e32 v[58:59], v[2:3]
	v_mov_b64_e32 v[66:67], v[2:3]
	v_mov_b64_e32 v[74:75], v[2:3]
	v_mov_b64_e32 v[82:83], v[2:3]
	v_mov_b64_e32 v[6:7], v[2:3]
	v_mov_b64_e32 v[10:11], v[2:3]
	v_mov_b64_e32 v[14:15], v[2:3]
	v_mov_b64_e32 v[22:23], v[2:3]
	v_mov_b64_e32 v[30:31], v[2:3]
	v_mov_b64_e32 v[38:39], v[2:3]
	v_mov_b64_e32 v[46:47], v[2:3]
	v_mov_b64_e32 v[54:55], v[2:3]
	v_mov_b64_e32 v[62:63], v[2:3]
	v_mov_b64_e32 v[70:71], v[2:3]
	v_mov_b64_e32 v[78:79], v[2:3]
	v_mov_b64_e32 v[86:87], v[2:3]
	v_mov_b64_e32 v[90:91], v[2:3]
	v_mov_b64_e32 v[94:95], v[2:3]
	v_mov_b64_e32 v[98:99], v[2:3]
	v_mov_b64_e32 v[102:103], v[2:3]
	v_mov_b32_e32 v156, v104
	v_mov_b64_e32 v[106:107], v[2:3]
	v_mov_b64_e32 v[110:111], v[2:3]
	v_mov_b64_e32 v[114:115], v[2:3]
	v_mov_b64_e32 v[118:119], v[2:3]
	v_mov_b64_e32 v[122:123], v[2:3]
	v_mov_b64_e32 v[126:127], v[2:3]
	s_mov_b64 s[20:21], 0x46000080
	s_mov_b32 s56, 0
	s_mov_b32 s51, 0x25800
	s_mov_b32 s52, 0x25c00
	s_add_i32 s53, 0, 0x10000
	s_add_i32 s54, 0, 0x14000
	s_mov_b64 s[22:23], 0x184000
	s_mov_b32 s55, 0x184000
	s_mov_b64 s[24:25], 0x4e000000
	v_mov_b64_e32 v[16:17], v[0:1]
	v_mov_b64_e32 v[24:25], v[0:1]
	v_mov_b64_e32 v[32:33], v[0:1]
	v_mov_b64_e32 v[40:41], v[0:1]
	v_mov_b64_e32 v[48:49], v[0:1]
	v_mov_b64_e32 v[56:57], v[0:1]
	v_mov_b64_e32 v[64:65], v[0:1]
	v_mov_b64_e32 v[72:73], v[0:1]
	v_mov_b64_e32 v[80:81], v[0:1]
	v_mov_b64_e32 v[4:5], v[0:1]
	v_mov_b64_e32 v[8:9], v[0:1]
	v_mov_b64_e32 v[12:13], v[0:1]
	v_mov_b64_e32 v[20:21], v[0:1]
	v_mov_b64_e32 v[28:29], v[0:1]
	v_mov_b64_e32 v[36:37], v[0:1]
	v_mov_b64_e32 v[44:45], v[0:1]
	v_mov_b64_e32 v[52:53], v[0:1]
	v_mov_b64_e32 v[60:61], v[0:1]
	v_mov_b64_e32 v[68:69], v[0:1]
	v_mov_b64_e32 v[76:77], v[0:1]
	v_mov_b64_e32 v[84:85], v[0:1]
	v_mov_b64_e32 v[88:89], v[0:1]
	v_mov_b64_e32 v[92:93], v[0:1]
	v_mov_b64_e32 v[96:97], v[0:1]
	v_mov_b64_e32 v[100:101], v[0:1]
	v_mov_b64_e32 v[104:105], v[0:1]
	v_mov_b64_e32 v[108:109], v[0:1]
	v_mov_b64_e32 v[112:113], v[0:1]
	v_mov_b64_e32 v[116:117], v[0:1]
	v_mov_b64_e32 v[120:121], v[0:1]
	v_mov_b64_e32 v[124:125], v[0:1]
	s_barrier
	s_branch .LBB0_625

.LBB0_637:
	s_add_u32 s64, s6, s36
	v_add_u32_e32 v142, s53, v175
	v_add_u32_e32 v154, s54, v175
	s_addc_u32 s65, s7, s37
	ds_read_b128 v[130:133], v142
	ds_read_b128 v[138:141], v142 offset:2048
	v_xor_b32_e32 v142, 64, v142
	ds_read_b128 v[134:137], v142
	ds_read_b128 v[142:145], v142 offset:2048
	ds_read_b128 v[146:149], v154
	ds_read_b128 v[168:171], v154 offset:2048
	v_xor_b32_e32 v154, 64, v154
	ds_read_b128 v[150:153], v154
	ds_read_b128 v[178:181], v154 offset:2048
	s_add_u32 s66, s64, 0x46000100
	s_addc_u32 s67, s65, 0
	s_and_b64 s[38:39], s[40:41], exec
	s_cselect_b32 s39, s13, s67
	s_cselect_b32 s38, s12, s66
	s_add_u32 s66, s27, s36
	s_addc_u32 s67, s59, s37
	s_and_b64 s[40:41], s[40:41], exec
	s_cselect_b32 s41, s31, s67
	s_cselect_b32 s40, s30, s66
	ds_read_b128 v[182:185], v176
	ds_read_b128 v[186:189], v177
	ds_read_b128 v[190:193], v176 offset:2048
	ds_read_b128 v[194:197], v177 offset:2048
	ds_read_b128 v[198:201], v176 offset:4096
	ds_read_b128 v[202:205], v177 offset:4096
	ds_read_b128 v[206:209], v176 offset:6144
	ds_read_b128 v[210:213], v177 offset:6144
	s_add_i32 m0, s11, 0xc000
	v_lshl_add_u64 v[154:155], s[64:65], 0, v[156:157]
	v_lshl_add_u64 v[154:155], v[154:155], 0, s[20:21]
	v_mov_b32_e32 v167, v157
	global_load_lds_dwordx4 v[154:155], off
	s_add_i32 m0, s11, 0xe000
	v_lshl_add_u64 v[154:155], s[64:65], 0, v[166:167]
	v_lshl_add_u64 v[154:155], v[154:155], 0, s[20:21]
	global_load_lds_dwordx4 v[154:155], off
	s_waitcnt vmcnt(8)
	s_waitcnt lgkmcnt(0)
	s_barrier
	s_setprio 1
	s_waitcnt lgkmcnt(0)
	v_mfma_f32_16x16x32_bf16 v[100:103], v[130:133], v[182:185], v[100:103]
	v_mfma_f32_16x16x32_bf16 v[96:99], v[138:141], v[182:185], v[96:99]
	v_mfma_f32_16x16x32_bf16 v[92:95], v[130:133], v[190:193], v[92:95]
	v_mfma_f32_16x16x32_bf16 v[88:91], v[138:141], v[190:193], v[88:91]
	v_mfma_f32_16x16x32_bf16 v[84:87], v[130:133], v[198:201], v[84:87]
	v_mfma_f32_16x16x32_bf16 v[76:79], v[138:141], v[198:201], v[76:79]
	v_mfma_f32_16x16x32_bf16 v[68:71], v[130:133], v[206:209], v[68:71]
	v_mfma_f32_16x16x32_bf16 v[60:63], v[138:141], v[206:209], v[60:63]
	v_mfma_f32_16x16x32_bf16 v[100:103], v[134:137], v[186:189], v[100:103]
	v_mfma_f32_16x16x32_bf16 v[96:99], v[142:145], v[186:189], v[96:99]
	v_mfma_f32_16x16x32_bf16 v[92:95], v[134:137], v[194:197], v[92:95]
	v_mfma_f32_16x16x32_bf16 v[88:91], v[142:145], v[194:197], v[88:91]
	v_mfma_f32_16x16x32_bf16 v[84:87], v[134:137], v[202:205], v[84:87]
	v_mfma_f32_16x16x32_bf16 v[76:79], v[142:145], v[202:205], v[76:79]
	v_mfma_f32_16x16x32_bf16 v[68:71], v[134:137], v[210:213], v[68:71]
	v_mfma_f32_16x16x32_bf16 v[60:63], v[142:145], v[210:213], v[60:63]
	s_setprio 0
	s_setprio 1
	v_mfma_f32_16x16x32_bf16 v[52:55], v[146:149], v[182:185], v[52:55]
	v_mfma_f32_16x16x32_bf16 v[44:47], v[168:171], v[182:185], v[44:47]
	v_mfma_f32_16x16x32_bf16 v[36:39], v[146:149], v[190:193], v[36:39]
	v_mfma_f32_16x16x32_bf16 v[28:31], v[168:171], v[190:193], v[28:31]
	v_mfma_f32_16x16x32_bf16 v[20:23], v[146:149], v[198:201], v[20:23]
	v_mfma_f32_16x16x32_bf16 v[12:15], v[168:171], v[198:201], v[12:15]
	v_mfma_f32_16x16x32_bf16 v[8:11], v[146:149], v[206:209], v[8:11]
	v_mfma_f32_16x16x32_bf16 v[4:7], v[168:171], v[206:209], v[4:7]
	v_mfma_f32_16x16x32_bf16 v[52:55], v[150:153], v[186:189], v[52:55]
	v_mfma_f32_16x16x32_bf16 v[44:47], v[178:181], v[186:189], v[44:47]
	v_mfma_f32_16x16x32_bf16 v[36:39], v[150:153], v[194:197], v[36:39]
	v_mfma_f32_16x16x32_bf16 v[28:31], v[178:181], v[194:197], v[28:31]
	v_mfma_f32_16x16x32_bf16 v[20:23], v[150:153], v[202:205], v[20:23]
	v_mfma_f32_16x16x32_bf16 v[12:15], v[178:181], v[202:205], v[12:15]
	v_mfma_f32_16x16x32_bf16 v[8:11], v[150:153], v[210:213], v[8:11]
	v_mfma_f32_16x16x32_bf16 v[4:7], v[178:181], v[210:213], v[4:7]
	s_setprio 0
	s_barrier
	s_add_i32 s64, s53, s42
	s_mov_b32 m0, s64
	ds_read_b128 v[182:185], v176 offset:16384
	ds_read_b128 v[186:189], v177 offset:16384
	ds_read_b128 v[190:193], v176 offset:18432
	ds_read_b128 v[194:197], v177 offset:18432
	ds_read_b128 v[198:201], v176 offset:20480
	ds_read_b128 v[202:205], v177 offset:20480
	ds_read_b128 v[206:209], v176 offset:22528
	ds_read_b128 v[210:213], v177 offset:22528
	s_nop 0
	global_load_lds_dwordx4 v164, s[40:41]
	s_add_i32 m0, s64, 0x2000
	s_add_u32 s64, s40, 0x8000
	s_addc_u32 s65, s41, 0
	s_add_i32 s66, s54, s42
	s_nop 0
	global_load_lds_dwordx4 v158, s[40:41]
	s_mov_b32 m0, s66
	s_nop 0
	global_load_lds_dwordx4 v164, s[64:65]
	s_add_i32 m0, s66, 0x2000
	s_nop 0
	global_load_lds_dwordx4 v158, s[64:65]
	s_waitcnt vmcnt(6)
	s_waitcnt lgkmcnt(0)
	s_barrier
	s_setprio 1
	s_waitcnt lgkmcnt(0)
	v_mfma_f32_16x16x32_bf16 v[80:83], v[130:133], v[182:185], v[80:83]
	v_mfma_f32_16x16x32_bf16 v[72:75], v[138:141], v[182:185], v[72:75]
	v_mfma_f32_16x16x32_bf16 v[64:67], v[130:133], v[190:193], v[64:67]
	v_mfma_f32_16x16x32_bf16 v[56:59], v[138:141], v[190:193], v[56:59]
	v_mfma_f32_16x16x32_bf16 v[48:51], v[130:133], v[198:201], v[48:51]
	v_mfma_f32_16x16x32_bf16 v[40:43], v[138:141], v[198:201], v[40:43]
	v_mfma_f32_16x16x32_bf16 v[32:35], v[130:133], v[206:209], v[32:35]
	v_mfma_f32_16x16x32_bf16 v[24:27], v[138:141], v[206:209], v[24:27]
	v_mfma_f32_16x16x32_bf16 v[80:83], v[134:137], v[186:189], v[80:83]
	v_mfma_f32_16x16x32_bf16 v[72:75], v[142:145], v[186:189], v[72:75]
	v_mfma_f32_16x16x32_bf16 v[64:67], v[134:137], v[194:197], v[64:67]
	v_mfma_f32_16x16x32_bf16 v[56:59], v[142:145], v[194:197], v[56:59]
	v_mfma_f32_16x16x32_bf16 v[48:51], v[134:137], v[202:205], v[48:51]
	v_mfma_f32_16x16x32_bf16 v[40:43], v[142:145], v[202:205], v[40:43]
	v_mfma_f32_16x16x32_bf16 v[32:35], v[134:137], v[210:213], v[32:35]
	v_mfma_f32_16x16x32_bf16 v[24:27], v[142:145], v[210:213], v[24:27]
	s_setprio 0
	s_setprio 1
	v_mfma_f32_16x16x32_bf16 v[16:19], v[146:149], v[182:185], v[16:19]
	v_mfma_f32_16x16x32_bf16 v[0:3], v[168:171], v[182:185], v[0:3]
	v_mfma_f32_16x16x32_bf16 v[104:107], v[146:149], v[190:193], v[104:107]
	v_mfma_f32_16x16x32_bf16 v[108:111], v[168:171], v[190:193], v[108:111]
	v_mfma_f32_16x16x32_bf16 v[112:115], v[146:149], v[198:201], v[112:115]
	v_mfma_f32_16x16x32_bf16 v[116:119], v[168:171], v[198:201], v[116:119]
	v_mfma_f32_16x16x32_bf16 v[120:123], v[146:149], v[206:209], v[120:123]
	v_mfma_f32_16x16x32_bf16 v[124:127], v[168:171], v[206:209], v[124:127]
	v_mfma_f32_16x16x32_bf16 v[16:19], v[150:153], v[186:189], v[16:19]
	v_mfma_f32_16x16x32_bf16 v[0:3], v[178:181], v[186:189], v[0:3]
	v_mfma_f32_16x16x32_bf16 v[104:107], v[150:153], v[194:197], v[104:107]
	v_mfma_f32_16x16x32_bf16 v[108:111], v[178:181], v[194:197], v[108:111]
	v_mfma_f32_16x16x32_bf16 v[112:115], v[150:153], v[202:205], v[112:115]
	v_mfma_f32_16x16x32_bf16 v[116:119], v[178:181], v[202:205], v[116:119]
	v_mfma_f32_16x16x32_bf16 v[120:123], v[150:153], v[210:213], v[120:123]
	v_mfma_f32_16x16x32_bf16 v[124:127], v[178:181], v[210:213], v[124:127]
	s_setprio 0
	s_barrier
	s_add_i32 s64, 0, 0x18000
	s_add_i32 s65, 0, 0x1c000
	v_add_u32_e32 v142, s64, v175
	v_add_u32_e32 v154, s65, v175
	ds_read_b128 v[130:133], v142
	ds_read_b128 v[138:141], v142 offset:2048
	v_xor_b32_e32 v142, 64, v142
	ds_read_b128 v[134:137], v142
	ds_read_b128 v[142:145], v142 offset:2048
	ds_read_b128 v[146:149], v154
	ds_read_b128 v[168:171], v154 offset:2048
	v_xor_b32_e32 v154, 64, v154
	ds_read_b128 v[150:153], v154
	ds_read_b128 v[178:181], v154 offset:2048
	s_mov_b32 m0, s45
	v_mov_b32_e32 v156, v129
	ds_read_b128 v[182:185], v176 offset:32768
	ds_read_b128 v[186:189], v177 offset:32768
	ds_read_b128 v[190:193], v176 offset:34816
	ds_read_b128 v[194:197], v177 offset:34816
	ds_read_b128 v[198:201], v176 offset:36864
	ds_read_b128 v[202:205], v177 offset:36864
	ds_read_b128 v[206:209], v176 offset:38912
	ds_read_b128 v[210:213], v177 offset:38912
	s_mov_b32 m0, s11
	s_nop 0
	global_load_lds_dwordx4 v160, s[38:39]
	s_mov_b32 m0, s44
	s_nop 0
	global_load_lds_dwordx4 v162, s[38:39]
	s_mov_b32 m0, s45
	v_mov_b32_e32 v166, v128
	global_load_lds_dwordx4 v156, s[38:39]
	s_mov_b32 m0, s46
	s_nop 0
	global_load_lds_dwordx4 v166, s[38:39]
	s_waitcnt vmcnt(8)
	s_waitcnt lgkmcnt(0)
	s_barrier
	s_setprio 1
	s_waitcnt lgkmcnt(0)
	v_mfma_f32_16x16x32_bf16 v[100:103], v[130:133], v[182:185], v[100:103]
	v_mfma_f32_16x16x32_bf16 v[96:99], v[138:141], v[182:185], v[96:99]
	v_mfma_f32_16x16x32_bf16 v[92:95], v[130:133], v[190:193], v[92:95]
	v_mfma_f32_16x16x32_bf16 v[88:91], v[138:141], v[190:193], v[88:91]
	v_mfma_f32_16x16x32_bf16 v[84:87], v[130:133], v[198:201], v[84:87]
	v_mfma_f32_16x16x32_bf16 v[76:79], v[138:141], v[198:201], v[76:79]
	v_mfma_f32_16x16x32_bf16 v[68:71], v[130:133], v[206:209], v[68:71]
	v_mfma_f32_16x16x32_bf16 v[60:63], v[138:141], v[206:209], v[60:63]
	v_mfma_f32_16x16x32_bf16 v[100:103], v[134:137], v[186:189], v[100:103]
	v_mfma_f32_16x16x32_bf16 v[96:99], v[142:145], v[186:189], v[96:99]
	v_mfma_f32_16x16x32_bf16 v[92:95], v[134:137], v[194:197], v[92:95]
	v_mfma_f32_16x16x32_bf16 v[88:91], v[142:145], v[194:197], v[88:91]
	v_mfma_f32_16x16x32_bf16 v[84:87], v[134:137], v[202:205], v[84:87]
	v_mfma_f32_16x16x32_bf16 v[76:79], v[142:145], v[202:205], v[76:79]
	v_mfma_f32_16x16x32_bf16 v[68:71], v[134:137], v[210:213], v[68:71]
	v_mfma_f32_16x16x32_bf16 v[60:63], v[142:145], v[210:213], v[60:63]
	s_setprio 0
	s_setprio 1
	v_mfma_f32_16x16x32_bf16 v[52:55], v[146:149], v[182:185], v[52:55]
	v_mfma_f32_16x16x32_bf16 v[44:47], v[168:171], v[182:185], v[44:47]
	v_mfma_f32_16x16x32_bf16 v[36:39], v[146:149], v[190:193], v[36:39]
	v_mfma_f32_16x16x32_bf16 v[28:31], v[168:171], v[190:193], v[28:31]
	v_mfma_f32_16x16x32_bf16 v[20:23], v[146:149], v[198:201], v[20:23]
	v_mfma_f32_16x16x32_bf16 v[12:15], v[168:171], v[198:201], v[12:15]
	v_mfma_f32_16x16x32_bf16 v[8:11], v[146:149], v[206:209], v[8:11]
	v_mfma_f32_16x16x32_bf16 v[4:7], v[168:171], v[206:209], v[4:7]
	v_mfma_f32_16x16x32_bf16 v[52:55], v[150:153], v[186:189], v[52:55]
	v_mfma_f32_16x16x32_bf16 v[44:47], v[178:181], v[186:189], v[44:47]
	v_mfma_f32_16x16x32_bf16 v[36:39], v[150:153], v[194:197], v[36:39]
	v_mfma_f32_16x16x32_bf16 v[28:31], v[178:181], v[194:197], v[28:31]
	v_mfma_f32_16x16x32_bf16 v[20:23], v[150:153], v[202:205], v[20:23]
	v_mfma_f32_16x16x32_bf16 v[12:15], v[178:181], v[202:205], v[12:15]
	v_mfma_f32_16x16x32_bf16 v[8:11], v[150:153], v[210:213], v[8:11]
	v_mfma_f32_16x16x32_bf16 v[4:7], v[178:181], v[210:213], v[4:7]
	s_setprio 0
	s_barrier
	v_mov_b32_e32 v165, v157
	ds_read_b128 v[182:185], v176 offset:49152
	ds_read_b128 v[186:189], v177 offset:49152
	ds_read_b128 v[190:193], v176 offset:51200
	ds_read_b128 v[194:197], v177 offset:51200
	ds_read_b128 v[198:201], v176 offset:53248
	ds_read_b128 v[202:205], v177 offset:53248
	ds_read_b128 v[206:209], v176 offset:55296
	ds_read_b128 v[210:213], v177 offset:55296
	s_add_i32 s64, s64, s42
	v_lshl_add_u64 v[128:129], s[40:41], 0, v[164:165]
	v_lshl_add_u64 v[128:129], v[128:129], 0, s[18:19]
	s_mov_b32 m0, s64
	v_mov_b32_e32 v159, v157
	global_load_lds_dwordx4 v[128:129], off
	s_add_i32 m0, s64, 0x2000
	v_mov_b32_e32 v161, v157
	v_lshl_add_u64 v[128:129], s[40:41], 0, v[158:159]
	s_add_u32 s40, s40, 0x8080
	v_lshl_add_u64 v[128:129], v[128:129], 0, s[18:19]
	s_addc_u32 s41, s41, 0
	s_add_i32 s64, s65, s42
	global_load_lds_dwordx4 v[128:129], off
	s_mov_b32 m0, s64
	v_mov_b32_e32 v163, v157
	global_load_lds_dwordx4 v164, s[40:41]
	s_add_i32 m0, s64, 0x2000
	s_nop 0
	global_load_lds_dwordx4 v158, s[40:41]
	s_mov_b32 m0, s49
	v_lshl_add_u64 v[128:129], s[38:39], 0, v[160:161]
	v_lshl_add_u64 v[128:129], v[128:129], 0, s[18:19]
	global_load_lds_dwordx4 v[128:129], off
	s_mov_b32 m0, s50
	v_lshl_add_u64 v[128:129], s[38:39], 0, v[162:163]
	v_lshl_add_u64 v[128:129], v[128:129], 0, s[18:19]
	global_load_lds_dwordx4 v[128:129], off
	s_waitcnt vmcnt(8)
	s_waitcnt lgkmcnt(0)
	s_barrier
	s_setprio 1
	s_waitcnt lgkmcnt(0)
	v_mfma_f32_16x16x32_bf16 v[80:83], v[130:133], v[182:185], v[80:83]
	v_mfma_f32_16x16x32_bf16 v[72:75], v[138:141], v[182:185], v[72:75]
	v_mfma_f32_16x16x32_bf16 v[64:67], v[130:133], v[190:193], v[64:67]
	v_mfma_f32_16x16x32_bf16 v[56:59], v[138:141], v[190:193], v[56:59]
	v_mfma_f32_16x16x32_bf16 v[48:51], v[130:133], v[198:201], v[48:51]
	v_mfma_f32_16x16x32_bf16 v[40:43], v[138:141], v[198:201], v[40:43]
	v_mfma_f32_16x16x32_bf16 v[32:35], v[130:133], v[206:209], v[32:35]
	v_mfma_f32_16x16x32_bf16 v[24:27], v[138:141], v[206:209], v[24:27]
	v_mfma_f32_16x16x32_bf16 v[80:83], v[134:137], v[186:189], v[80:83]
	v_mfma_f32_16x16x32_bf16 v[72:75], v[142:145], v[186:189], v[72:75]
	v_mfma_f32_16x16x32_bf16 v[64:67], v[134:137], v[194:197], v[64:67]
	v_mfma_f32_16x16x32_bf16 v[56:59], v[142:145], v[194:197], v[56:59]
	v_mfma_f32_16x16x32_bf16 v[48:51], v[134:137], v[202:205], v[48:51]
	v_mfma_f32_16x16x32_bf16 v[40:43], v[142:145], v[202:205], v[40:43]
	v_mfma_f32_16x16x32_bf16 v[32:35], v[134:137], v[210:213], v[32:35]
	v_mfma_f32_16x16x32_bf16 v[24:27], v[142:145], v[210:213], v[24:27]
	s_setprio 0
	s_setprio 1
	v_mfma_f32_16x16x32_bf16 v[16:19], v[146:149], v[182:185], v[16:19]
	v_mfma_f32_16x16x32_bf16 v[0:3], v[168:171], v[182:185], v[0:3]
	v_mfma_f32_16x16x32_bf16 v[104:107], v[146:149], v[190:193], v[104:107]
	v_mfma_f32_16x16x32_bf16 v[108:111], v[168:171], v[190:193], v[108:111]
	v_mfma_f32_16x16x32_bf16 v[112:115], v[146:149], v[198:201], v[112:115]
	v_mfma_f32_16x16x32_bf16 v[116:119], v[168:171], v[198:201], v[116:119]
	v_mfma_f32_16x16x32_bf16 v[120:123], v[146:149], v[206:209], v[120:123]
	v_mfma_f32_16x16x32_bf16 v[124:127], v[168:171], v[206:209], v[124:127]
	v_mfma_f32_16x16x32_bf16 v[16:19], v[150:153], v[186:189], v[16:19]
	v_mfma_f32_16x16x32_bf16 v[0:3], v[178:181], v[186:189], v[0:3]
	v_mfma_f32_16x16x32_bf16 v[104:107], v[150:153], v[194:197], v[104:107]
	v_mfma_f32_16x16x32_bf16 v[108:111], v[178:181], v[194:197], v[108:111]
	v_mfma_f32_16x16x32_bf16 v[112:115], v[150:153], v[202:205], v[112:115]
	v_mfma_f32_16x16x32_bf16 v[116:119], v[178:181], v[202:205], v[116:119]
	v_mfma_f32_16x16x32_bf16 v[120:123], v[150:153], v[210:213], v[120:123]
	v_mfma_f32_16x16x32_bf16 v[124:127], v[178:181], v[210:213], v[124:127]
	s_setprio 0
	s_barrier
	s_add_i32 s63, s63, 2
	s_add_u32 s36, s36, 0x100
	s_addc_u32 s37, s37, 0
	s_cmp_gt_u32 s63, 29
	s_cbranch_scc1 .LBB0_642

.LBB0_640:
	s_cmpk_eq_i32 s36, 0xf00
	s_cselect_b64 s[40:41], -1, 0
	s_and_b64 s[38:39], s[34:35], s[40:41]
	s_andn2_b64 vcc, exec, s[38:39]
	v_mov_b32_e32 v128, v166
	v_mov_b32_e32 v129, v156
	s_cbranch_vccnz .LBB0_637
	v_mbcnt_lo_u32_b32 v128, -1, 0
	v_mbcnt_hi_u32_b32 v128, -1, v128
	v_and_b32_e32 v130, 7, v128
	v_add_u32_e32 v128, s33, v128
	v_lshrrev_b32_e32 v131, 3, v128
	v_bfe_u32 v128, v131, 1, 3
	v_and_b32_e32 v129, 1, v128
	v_lshlrev_b32_e32 v129, 1, v129
	v_and_or_b32 v128, v128, 4, v129
	v_xor_b32_e32 v130, v130, v128
	v_lshlrev_b32_e32 v130, 4, v130
	v_add_u32_e32 v132, 64, v131
	v_lshlrev_b32_e32 v129, 12, v131
	v_add3_u32 v160, v129, s61, v130
	v_lshlrev_b32_e32 v129, 12, v132
	v_add3_u32 v162, v129, s61, v130
	v_add_u32_e32 v129, s62, v131
	v_lshl_add_u32 v129, v129, 12, v130
	v_add_u32_e32 v128, s62, v132
	v_lshl_add_u32 v128, v128, 12, v130
	s_branch .LBB0_637
